# P3 epilogue: the 8 CQSS row loads hoisted and waited once (was load+vmcnt(0) per group behind the previous group's stores); P2 rf-tile redundant vmcnt(0) dropped; masked indexer loop K-prefetch wait m
# baseline (speedup 1.0000x reference)
.LBB0_338:
	s_ashr_i32 s15, s14, 31
	s_lshl_b64 s[0:1], s[14:15], 26
	s_add_u32 s0, s61, s0
	s_addc_u32 s1, s62, s1
	v_lshlrev_b32_e32 v146, 1, v146
	v_ashrrev_i32_e32 v169, 31, v168
	v_lshl_add_u64 v[184:185], s[0:1], 0, v[146:147]
	v_cvt_pk_bf16_f32 v178, v170, v171
	v_lshlrev_b64 v[170:171], 10, v[168:169]
	v_cndmask_b32_e64 v146, 0, 1, s[52:53]
	v_cvt_pk_bf16_f32 v179, v174, v175
	v_lshl_add_u64 v[170:171], v[184:185], 0, v[170:171]
	v_cmp_ne_u32_e64 s[12:13], 1, v146
	s_andn2_b64 vcc, exec, s[52:53]
	s_mov_b64 s[0:1], -1
	v_cvt_pk_bf16_f32 v180, v172, v173
	v_cvt_pk_bf16_f32 v181, v176, v177
	global_store_dwordx4 v[170:171], v[178:181], off
	s_cbranch_vccnz .LBB0_342
	s_and_b64 vcc, exec, s[10:11]
	v_mov_b32_e32 v179, v109
	v_mov_b32_e32 v178, v108
	v_mov_b32_e32 v175, v107
	v_mov_b32_e32 v174, v106
	v_mov_b32_e32 v177, v113
	v_mov_b32_e32 v176, v112
	v_mov_b32_e32 v173, v111
	v_mov_b32_e32 v172, v110
	s_cbranch_vccnz .LBB0_341
	v_mul_f32_e32 v146, 0xbfb8aa3b, v110
	v_exp_f32_e32 v146, v146
	v_mul_f32_e32 v172, 0xbfb8aa3b, v106
	v_exp_f32_e32 v172, v172
	v_sub_f32_e32 v173, 1.0, v134
	v_add_f32_e32 v146, 1.0, v146
	v_rcp_f32_e32 v146, v146
	v_add_f32_e32 v172, 1.0, v172
	v_rcp_f32_e32 v172, v172
	v_sub_f32_e32 v175, 1.0, v135
	v_fma_f32 v146, v146, v173, v134
	v_cmp_gt_f32_e32 vcc, s70, v146
	v_sub_f32_e32 v176, 1.0, v131
	v_sub_f32_e32 v177, 1.0, v136
	v_cndmask_b32_e64 v173, 0, 32, vcc
	v_ldexp_f32 v146, v146, v173
	v_log_f32_e32 v146, v146
	v_sub_f32_e32 v173, 1.0, v130
	v_fma_f32 v172, v172, v173, v130
	v_cmp_gt_f32_e64 s[0:1], s70, v172
	v_mul_f32_e32 v173, 0x3f317217, v146
	v_fma_f32 v173, v146, s71, -v173
	v_fmac_f32_e32 v173, 0x3377d1cf, v146
	v_fmac_f32_e32 v173, 0x3f317217, v146
	v_cmp_lt_f32_e64 s[14:15], |v146|, s72
	v_cndmask_b32_e64 v174, 0, 32, s[0:1]
	v_ldexp_f32 v172, v172, v174
	v_cndmask_b32_e64 v146, v146, v173, s[14:15]
	v_mul_f32_e32 v173, 0xbfb8aa3b, v111
	v_exp_f32_e32 v173, v173
	v_log_f32_e32 v174, v172
	v_cndmask_b32_e32 v172, 0, v201, vcc
	v_sub_f32_e32 v172, v146, v172
	v_add_f32_e32 v173, 1.0, v173
	v_rcp_f32_e32 v173, v173
	v_mul_f32_e32 v146, 0x3f317217, v174
	v_fma_f32 v146, v174, s71, -v146
	v_fmac_f32_e32 v146, 0x3377d1cf, v174
	v_fmac_f32_e32 v146, 0x3f317217, v174
	v_cmp_lt_f32_e64 vcc, |v174|, s72
	v_fma_f32 v173, v173, v175, v135
	v_sub_f32_e32 v178, 1.0, v132
	v_cndmask_b32_e32 v146, v174, v146, vcc
	v_cmp_gt_f32_e32 vcc, s70, v173
	v_cndmask_b32_e64 v174, 0, v201, s[0:1]
	v_sub_f32_e32 v174, v146, v174
	v_cndmask_b32_e64 v175, 0, 32, vcc
	v_ldexp_f32 v173, v173, v175
	v_mul_f32_e32 v175, 0xbfb8aa3b, v107
	v_exp_f32_e32 v175, v175
	v_log_f32_e32 v173, v173
	v_sub_f32_e32 v179, 1.0, v137
	v_add_f32_e32 v175, 1.0, v175
	v_rcp_f32_e32 v175, v175
	v_mul_f32_e32 v146, 0x3f317217, v173
	v_fma_f32 v146, v173, s71, -v146
	v_fmac_f32_e32 v146, 0x3377d1cf, v173
	v_fma_f32 v175, v175, v176, v131
	v_cmp_gt_f32_e64 s[0:1], s70, v175
	v_fmac_f32_e32 v146, 0x3f317217, v173
	v_cmp_lt_f32_e64 s[14:15], |v173|, s72
	v_cndmask_b32_e64 v176, 0, 32, s[0:1]
	v_ldexp_f32 v175, v175, v176
	v_mul_f32_e32 v176, 0xbfb8aa3b, v112
	v_exp_f32_e32 v176, v176
	v_log_f32_e32 v175, v175
	v_cndmask_b32_e64 v146, v173, v146, s[14:15]
	v_cndmask_b32_e32 v173, 0, v201, vcc
	v_add_f32_e32 v176, 1.0, v176
	v_rcp_f32_e32 v176, v176
	v_sub_f32_e32 v173, v146, v173
	v_mul_f32_e32 v146, 0x3f317217, v175
	v_fma_f32 v146, v175, s71, -v146
	v_fmac_f32_e32 v146, 0x3377d1cf, v175
	v_fmac_f32_e32 v146, 0x3f317217, v175
	v_cmp_lt_f32_e64 vcc, |v175|, s72
	v_fma_f32 v176, v176, v177, v136
	s_nop 0
	v_cndmask_b32_e32 v146, v175, v146, vcc
	v_cmp_gt_f32_e32 vcc, s70, v176
	v_cndmask_b32_e64 v175, 0, v201, s[0:1]
	v_sub_f32_e32 v175, v146, v175
	v_cndmask_b32_e64 v177, 0, 32, vcc
	v_ldexp_f32 v176, v176, v177
	v_mul_f32_e32 v177, 0xbfb8aa3b, v108
	v_exp_f32_e32 v177, v177
	v_log_f32_e32 v176, v176
	v_add_f32_e32 v177, 1.0, v177
	v_rcp_f32_e32 v177, v177
	v_mul_f32_e32 v146, 0x3f317217, v176
	v_fma_f32 v146, v176, s71, -v146
	v_fmac_f32_e32 v146, 0x3377d1cf, v176
	v_fma_f32 v177, v177, v178, v132
	v_cmp_gt_f32_e64 s[0:1], s70, v177
	v_fmac_f32_e32 v146, 0x3f317217, v176
	v_cmp_lt_f32_e64 s[14:15], |v176|, s72
	v_cndmask_b32_e64 v178, 0, 32, s[0:1]
	v_ldexp_f32 v177, v177, v178
	v_mul_f32_e32 v178, 0xbfb8aa3b, v113
	v_exp_f32_e32 v178, v178
	v_log_f32_e32 v177, v177
	v_cndmask_b32_e64 v146, v176, v146, s[14:15]
	v_cndmask_b32_e32 v176, 0, v201, vcc
	v_add_f32_e32 v178, 1.0, v178
	v_rcp_f32_e32 v178, v178
	v_sub_f32_e32 v176, v146, v176
	v_mul_f32_e32 v146, 0x3f317217, v177
	v_fma_f32 v146, v177, s71, -v146
	v_fmac_f32_e32 v146, 0x3377d1cf, v177
	v_fmac_f32_e32 v146, 0x3f317217, v177
	v_cmp_lt_f32_e64 vcc, |v177|, s72
	v_fma_f32 v178, v178, v179, v137
	s_nop 0
	v_cndmask_b32_e32 v146, v177, v146, vcc
	v_cmp_gt_f32_e32 vcc, s70, v178
	v_cndmask_b32_e64 v177, 0, v201, s[0:1]
	s_nop 0
	v_cndmask_b32_e64 v179, 0, 32, vcc
	v_ldexp_f32 v178, v178, v179
	v_log_f32_e32 v179, v178
	v_mul_f32_e32 v178, 0xbfb8aa3b, v109
	v_exp_f32_e32 v180, v178
	v_sub_f32_e32 v178, v146, v177
	v_mul_f32_e32 v146, 0x3f317217, v179
	v_fma_f32 v146, v179, s71, -v146
	v_add_f32_e32 v177, 1.0, v180
	v_rcp_f32_e32 v177, v177
	v_sub_f32_e32 v180, 1.0, v133
	v_fmac_f32_e32 v146, 0x3377d1cf, v179
	v_fmac_f32_e32 v146, 0x3f317217, v179
	v_fma_f32 v177, v177, v180, v133
	v_cmp_gt_f32_e64 s[0:1], s70, v177
	v_cmp_lt_f32_e64 s[14:15], |v179|, s72
	s_nop 0
	v_cndmask_b32_e64 v180, 0, 32, s[0:1]
	v_ldexp_f32 v177, v177, v180
	v_log_f32_e32 v180, v177
	v_cndmask_b32_e64 v146, v179, v146, s[14:15]
	v_cndmask_b32_e32 v177, 0, v201, vcc
	v_sub_f32_e32 v177, v146, v177
	v_mul_f32_e32 v146, 0x3f317217, v180
	v_fma_f32 v146, v180, s71, -v146
	v_fmac_f32_e32 v146, 0x3377d1cf, v180
	v_fmac_f32_e32 v146, 0x3f317217, v180
	v_cmp_lt_f32_e64 vcc, |v180|, s72
	v_cndmask_b32_e64 v179, 0, v201, s[0:1]
	s_nop 0
	v_cndmask_b32_e32 v146, v180, v146, vcc
	v_sub_f32_e32 v179, v146, v179

.LBB0_344:
	v_or_b32_e32 v186, 16, v168
	v_ashrrev_i32_e32 v187, 31, v186
	v_cvt_pk_bf16_f32 v180, v172, v173
	v_lshlrev_b64 v[172:173], 10, v[186:187]
	v_cvt_pk_bf16_f32 v181, v176, v177
	v_lshl_add_u64 v[172:173], v[184:185], 0, v[172:173]
	s_and_b64 vcc, exec, s[12:13]
	s_mov_b64 s[0:1], -1
	v_cvt_pk_bf16_f32 v182, v174, v175
	v_cvt_pk_bf16_f32 v183, v178, v179
	global_store_dwordx4 v[172:173], v[180:183], off
	s_cbranch_vccnz .LBB0_348
	s_and_b64 vcc, exec, s[10:11]
	v_mov_b32_e32 v181, v93
	v_mov_b32_e32 v180, v92
	v_mov_b32_e32 v177, v91
	v_mov_b32_e32 v176, v90
	v_mov_b32_e32 v179, v97
	v_mov_b32_e32 v178, v96
	v_mov_b32_e32 v175, v95
	v_mov_b32_e32 v174, v94
	s_cbranch_vccnz .LBB0_347
	v_mul_f32_e32 v146, 0xbfb8aa3b, v94
	v_exp_f32_e32 v146, v146
	v_mul_f32_e32 v174, 0xbfb8aa3b, v90
	v_exp_f32_e32 v174, v174
	v_sub_f32_e32 v175, 1.0, v134
	v_add_f32_e32 v146, 1.0, v146
	v_rcp_f32_e32 v146, v146
	v_add_f32_e32 v174, 1.0, v174
	v_rcp_f32_e32 v174, v174
	v_sub_f32_e32 v177, 1.0, v135
	v_fma_f32 v146, v146, v175, v134
	v_cmp_gt_f32_e32 vcc, s70, v146
	v_sub_f32_e32 v178, 1.0, v131
	v_sub_f32_e32 v179, 1.0, v136
	v_cndmask_b32_e64 v175, 0, 32, vcc
	v_ldexp_f32 v146, v146, v175
	v_log_f32_e32 v146, v146
	v_sub_f32_e32 v175, 1.0, v130
	v_fma_f32 v174, v174, v175, v130
	v_cmp_gt_f32_e64 s[0:1], s70, v174
	v_mul_f32_e32 v175, 0x3f317217, v146
	v_fma_f32 v175, v146, s71, -v175
	v_fmac_f32_e32 v175, 0x3377d1cf, v146
	v_fmac_f32_e32 v175, 0x3f317217, v146
	v_cmp_lt_f32_e64 s[14:15], |v146|, s72
	v_cndmask_b32_e64 v176, 0, 32, s[0:1]
	v_ldexp_f32 v174, v174, v176
	v_cndmask_b32_e64 v146, v146, v175, s[14:15]
	v_mul_f32_e32 v175, 0xbfb8aa3b, v95
	v_exp_f32_e32 v175, v175
	v_log_f32_e32 v176, v174
	v_cndmask_b32_e32 v174, 0, v201, vcc
	v_sub_f32_e32 v174, v146, v174
	v_add_f32_e32 v175, 1.0, v175
	v_rcp_f32_e32 v175, v175
	v_mul_f32_e32 v146, 0x3f317217, v176
	v_fma_f32 v146, v176, s71, -v146
	v_fmac_f32_e32 v146, 0x3377d1cf, v176
	v_fmac_f32_e32 v146, 0x3f317217, v176
	v_cmp_lt_f32_e64 vcc, |v176|, s72
	v_fma_f32 v175, v175, v177, v135
	v_sub_f32_e32 v180, 1.0, v132
	v_cndmask_b32_e32 v146, v176, v146, vcc
	v_cmp_gt_f32_e32 vcc, s70, v175
	v_cndmask_b32_e64 v176, 0, v201, s[0:1]
	v_sub_f32_e32 v176, v146, v176
	v_cndmask_b32_e64 v177, 0, 32, vcc
	v_ldexp_f32 v175, v175, v177
	v_mul_f32_e32 v177, 0xbfb8aa3b, v91
	v_exp_f32_e32 v177, v177
	v_log_f32_e32 v175, v175
	v_sub_f32_e32 v181, 1.0, v137
	v_add_f32_e32 v177, 1.0, v177
	v_rcp_f32_e32 v177, v177
	v_mul_f32_e32 v146, 0x3f317217, v175
	v_fma_f32 v146, v175, s71, -v146
	v_fmac_f32_e32 v146, 0x3377d1cf, v175
	v_fma_f32 v177, v177, v178, v131
	v_cmp_gt_f32_e64 s[0:1], s70, v177
	v_fmac_f32_e32 v146, 0x3f317217, v175
	v_cmp_lt_f32_e64 s[14:15], |v175|, s72
	v_cndmask_b32_e64 v178, 0, 32, s[0:1]
	v_ldexp_f32 v177, v177, v178
	v_mul_f32_e32 v178, 0xbfb8aa3b, v96
	v_exp_f32_e32 v178, v178
	v_log_f32_e32 v177, v177
	v_cndmask_b32_e64 v146, v175, v146, s[14:15]
	v_cndmask_b32_e32 v175, 0, v201, vcc
	v_add_f32_e32 v178, 1.0, v178
	v_rcp_f32_e32 v178, v178
	v_sub_f32_e32 v175, v146, v175
	v_mul_f32_e32 v146, 0x3f317217, v177
	v_fma_f32 v146, v177, s71, -v146
	v_fmac_f32_e32 v146, 0x3377d1cf, v177
	v_fmac_f32_e32 v146, 0x3f317217, v177
	v_cmp_lt_f32_e64 vcc, |v177|, s72
	v_fma_f32 v178, v178, v179, v136
	s_nop 0
	v_cndmask_b32_e32 v146, v177, v146, vcc
	v_cmp_gt_f32_e32 vcc, s70, v178
	v_cndmask_b32_e64 v177, 0, v201, s[0:1]
	v_sub_f32_e32 v177, v146, v177
	v_cndmask_b32_e64 v179, 0, 32, vcc
	v_ldexp_f32 v178, v178, v179
	v_mul_f32_e32 v179, 0xbfb8aa3b, v92
	v_exp_f32_e32 v179, v179
	v_log_f32_e32 v178, v178
	v_add_f32_e32 v179, 1.0, v179
	v_rcp_f32_e32 v179, v179
	v_mul_f32_e32 v146, 0x3f317217, v178
	v_fma_f32 v146, v178, s71, -v146
	v_fmac_f32_e32 v146, 0x3377d1cf, v178
	v_fma_f32 v179, v179, v180, v132
	v_cmp_gt_f32_e64 s[0:1], s70, v179
	v_fmac_f32_e32 v146, 0x3f317217, v178
	v_cmp_lt_f32_e64 s[14:15], |v178|, s72
	v_cndmask_b32_e64 v180, 0, 32, s[0:1]
	v_ldexp_f32 v179, v179, v180
	v_mul_f32_e32 v180, 0xbfb8aa3b, v97
	v_exp_f32_e32 v180, v180
	v_log_f32_e32 v179, v179
	v_cndmask_b32_e64 v146, v178, v146, s[14:15]
	v_cndmask_b32_e32 v178, 0, v201, vcc
	v_add_f32_e32 v180, 1.0, v180
	v_rcp_f32_e32 v180, v180
	v_sub_f32_e32 v178, v146, v178
	v_mul_f32_e32 v146, 0x3f317217, v179
	v_fma_f32 v146, v179, s71, -v146
	v_fmac_f32_e32 v146, 0x3377d1cf, v179
	v_fmac_f32_e32 v146, 0x3f317217, v179
	v_cmp_lt_f32_e64 vcc, |v179|, s72
	v_fma_f32 v180, v180, v181, v137
	s_nop 0
	v_cndmask_b32_e32 v146, v179, v146, vcc
	v_cmp_gt_f32_e32 vcc, s70, v180
	v_cndmask_b32_e64 v179, 0, v201, s[0:1]
	s_nop 0
	v_cndmask_b32_e64 v181, 0, 32, vcc
	v_ldexp_f32 v180, v180, v181
	v_log_f32_e32 v181, v180
	v_mul_f32_e32 v180, 0xbfb8aa3b, v93
	v_exp_f32_e32 v182, v180
	v_sub_f32_e32 v180, v146, v179
	v_mul_f32_e32 v146, 0x3f317217, v181
	v_fma_f32 v146, v181, s71, -v146
	v_add_f32_e32 v179, 1.0, v182
	v_rcp_f32_e32 v179, v179
	v_sub_f32_e32 v182, 1.0, v133
	v_fmac_f32_e32 v146, 0x3377d1cf, v181
	v_fmac_f32_e32 v146, 0x3f317217, v181
	v_fma_f32 v179, v179, v182, v133
	v_cmp_gt_f32_e64 s[0:1], s70, v179
	v_cmp_lt_f32_e64 s[14:15], |v181|, s72
	s_nop 0
	v_cndmask_b32_e64 v182, 0, 32, s[0:1]
	v_ldexp_f32 v179, v179, v182
	v_log_f32_e32 v182, v179
	v_cndmask_b32_e64 v146, v181, v146, s[14:15]
	v_cndmask_b32_e32 v179, 0, v201, vcc
	v_sub_f32_e32 v179, v146, v179
	v_mul_f32_e32 v146, 0x3f317217, v182
	v_fma_f32 v146, v182, s71, -v146
	v_fmac_f32_e32 v146, 0x3377d1cf, v182
	v_fmac_f32_e32 v146, 0x3f317217, v182
	v_cmp_lt_f32_e64 vcc, |v182|, s72
	v_cndmask_b32_e64 v181, 0, v201, s[0:1]
	s_nop 0
	v_cndmask_b32_e32 v146, v182, v146, vcc
	v_sub_f32_e32 v181, v146, v181

.LBB0_350:
	v_or_b32_e32 v182, 32, v168
	v_ashrrev_i32_e32 v183, 31, v182
	v_cvt_pk_bf16_f32 v186, v174, v175
	v_lshlrev_b64 v[174:175], 10, v[182:183]
	v_lshl_add_u64 v[174:175], v[184:185], 0, v[174:175]
	s_and_b64 vcc, exec, s[12:13]
	s_mov_b64 s[0:1], -1
	v_cvt_pk_bf16_f32 v187, v178, v179
	v_cvt_pk_bf16_f32 v188, v176, v177
	v_cvt_pk_bf16_f32 v189, v180, v181
	global_store_dwordx4 v[174:175], v[186:189], off
	s_cbranch_vccnz .LBB0_354
	s_and_b64 vcc, exec, s[10:11]
	v_mov_b32_e32 v183, v77
	v_mov_b32_e32 v182, v76
	v_mov_b32_e32 v179, v75
	v_mov_b32_e32 v178, v74
	v_mov_b32_e32 v181, v81
	v_mov_b32_e32 v180, v80
	v_mov_b32_e32 v177, v79
	v_mov_b32_e32 v176, v78
	s_cbranch_vccnz .LBB0_353
	v_mul_f32_e32 v146, 0xbfb8aa3b, v78
	v_exp_f32_e32 v146, v146
	v_mul_f32_e32 v176, 0xbfb8aa3b, v74
	v_exp_f32_e32 v176, v176
	v_sub_f32_e32 v177, 1.0, v134
	v_add_f32_e32 v146, 1.0, v146
	v_rcp_f32_e32 v146, v146
	v_add_f32_e32 v176, 1.0, v176
	v_rcp_f32_e32 v176, v176
	v_sub_f32_e32 v179, 1.0, v135
	v_fma_f32 v146, v146, v177, v134
	v_cmp_gt_f32_e32 vcc, s70, v146
	v_sub_f32_e32 v180, 1.0, v131
	v_sub_f32_e32 v181, 1.0, v136
	v_cndmask_b32_e64 v177, 0, 32, vcc
	v_ldexp_f32 v146, v146, v177
	v_log_f32_e32 v146, v146
	v_sub_f32_e32 v177, 1.0, v130
	v_fma_f32 v176, v176, v177, v130
	v_cmp_gt_f32_e64 s[0:1], s70, v176
	v_mul_f32_e32 v177, 0x3f317217, v146
	v_fma_f32 v177, v146, s71, -v177
	v_fmac_f32_e32 v177, 0x3377d1cf, v146
	v_fmac_f32_e32 v177, 0x3f317217, v146
	v_cmp_lt_f32_e64 s[14:15], |v146|, s72
	v_cndmask_b32_e64 v178, 0, 32, s[0:1]
	v_ldexp_f32 v176, v176, v178
	v_cndmask_b32_e64 v146, v146, v177, s[14:15]
	v_mul_f32_e32 v177, 0xbfb8aa3b, v79
	v_exp_f32_e32 v177, v177
	v_log_f32_e32 v178, v176
	v_cndmask_b32_e32 v176, 0, v201, vcc
	v_sub_f32_e32 v176, v146, v176
	v_add_f32_e32 v177, 1.0, v177
	v_rcp_f32_e32 v177, v177
	v_mul_f32_e32 v146, 0x3f317217, v178
	v_fma_f32 v146, v178, s71, -v146
	v_fmac_f32_e32 v146, 0x3377d1cf, v178
	v_fmac_f32_e32 v146, 0x3f317217, v178
	v_cmp_lt_f32_e64 vcc, |v178|, s72
	v_fma_f32 v177, v177, v179, v135
	v_sub_f32_e32 v182, 1.0, v132
	v_cndmask_b32_e32 v146, v178, v146, vcc
	v_cmp_gt_f32_e32 vcc, s70, v177
	v_cndmask_b32_e64 v178, 0, v201, s[0:1]
	v_sub_f32_e32 v178, v146, v178
	v_cndmask_b32_e64 v179, 0, 32, vcc
	v_ldexp_f32 v177, v177, v179
	v_mul_f32_e32 v179, 0xbfb8aa3b, v75
	v_exp_f32_e32 v179, v179
	v_log_f32_e32 v177, v177
	v_sub_f32_e32 v183, 1.0, v137
	v_add_f32_e32 v179, 1.0, v179
	v_rcp_f32_e32 v179, v179
	v_mul_f32_e32 v146, 0x3f317217, v177
	v_fma_f32 v146, v177, s71, -v146
	v_fmac_f32_e32 v146, 0x3377d1cf, v177
	v_fma_f32 v179, v179, v180, v131
	v_cmp_gt_f32_e64 s[0:1], s70, v179
	v_fmac_f32_e32 v146, 0x3f317217, v177
	v_cmp_lt_f32_e64 s[14:15], |v177|, s72
	v_cndmask_b32_e64 v180, 0, 32, s[0:1]
	v_ldexp_f32 v179, v179, v180
	v_mul_f32_e32 v180, 0xbfb8aa3b, v80
	v_exp_f32_e32 v180, v180
	v_log_f32_e32 v179, v179
	v_cndmask_b32_e64 v146, v177, v146, s[14:15]
	v_cndmask_b32_e32 v177, 0, v201, vcc
	v_add_f32_e32 v180, 1.0, v180
	v_rcp_f32_e32 v180, v180
	v_sub_f32_e32 v177, v146, v177
	v_mul_f32_e32 v146, 0x3f317217, v179
	v_fma_f32 v146, v179, s71, -v146
	v_fmac_f32_e32 v146, 0x3377d1cf, v179
	v_fmac_f32_e32 v146, 0x3f317217, v179
	v_cmp_lt_f32_e64 vcc, |v179|, s72
	v_fma_f32 v180, v180, v181, v136
	s_nop 0
	v_cndmask_b32_e32 v146, v179, v146, vcc
	v_cmp_gt_f32_e32 vcc, s70, v180
	v_cndmask_b32_e64 v179, 0, v201, s[0:1]
	v_sub_f32_e32 v179, v146, v179
	v_cndmask_b32_e64 v181, 0, 32, vcc
	v_ldexp_f32 v180, v180, v181
	v_mul_f32_e32 v181, 0xbfb8aa3b, v76
	v_exp_f32_e32 v181, v181
	v_log_f32_e32 v180, v180
	v_add_f32_e32 v181, 1.0, v181
	v_rcp_f32_e32 v181, v181
	v_mul_f32_e32 v146, 0x3f317217, v180
	v_fma_f32 v146, v180, s71, -v146
	v_fmac_f32_e32 v146, 0x3377d1cf, v180
	v_fma_f32 v181, v181, v182, v132
	v_cmp_gt_f32_e64 s[0:1], s70, v181
	v_fmac_f32_e32 v146, 0x3f317217, v180
	v_cmp_lt_f32_e64 s[14:15], |v180|, s72
	v_cndmask_b32_e64 v182, 0, 32, s[0:1]
	v_ldexp_f32 v181, v181, v182
	v_mul_f32_e32 v182, 0xbfb8aa3b, v81
	v_exp_f32_e32 v182, v182
	v_log_f32_e32 v181, v181
	v_cndmask_b32_e64 v146, v180, v146, s[14:15]
	v_cndmask_b32_e32 v180, 0, v201, vcc
	v_add_f32_e32 v182, 1.0, v182
	v_rcp_f32_e32 v182, v182
	v_sub_f32_e32 v180, v146, v180
	v_mul_f32_e32 v146, 0x3f317217, v181
	v_fma_f32 v146, v181, s71, -v146
	v_fmac_f32_e32 v146, 0x3377d1cf, v181
	v_fmac_f32_e32 v146, 0x3f317217, v181
	v_cmp_lt_f32_e64 vcc, |v181|, s72
	v_fma_f32 v182, v182, v183, v137
	s_nop 0
	v_cndmask_b32_e32 v146, v181, v146, vcc
	v_cmp_gt_f32_e32 vcc, s70, v182
	v_cndmask_b32_e64 v181, 0, v201, s[0:1]
	s_nop 0
	v_cndmask_b32_e64 v183, 0, 32, vcc
	v_ldexp_f32 v182, v182, v183
	v_log_f32_e32 v183, v182
	v_mul_f32_e32 v182, 0xbfb8aa3b, v77
	v_exp_f32_e32 v186, v182
	v_sub_f32_e32 v182, v146, v181
	v_mul_f32_e32 v146, 0x3f317217, v183
	v_fma_f32 v146, v183, s71, -v146
	v_add_f32_e32 v181, 1.0, v186
	v_rcp_f32_e32 v181, v181
	v_sub_f32_e32 v186, 1.0, v133
	v_fmac_f32_e32 v146, 0x3377d1cf, v183
	v_fmac_f32_e32 v146, 0x3f317217, v183
	v_fma_f32 v181, v181, v186, v133
	v_cmp_gt_f32_e64 s[0:1], s70, v181
	v_cmp_lt_f32_e64 s[14:15], |v183|, s72
	s_nop 0
	v_cndmask_b32_e64 v186, 0, 32, s[0:1]
	v_ldexp_f32 v181, v181, v186
	v_log_f32_e32 v186, v181
	v_cndmask_b32_e64 v146, v183, v146, s[14:15]
	v_cndmask_b32_e32 v181, 0, v201, vcc
	v_sub_f32_e32 v181, v146, v181
	v_mul_f32_e32 v146, 0x3f317217, v186
	v_fma_f32 v146, v186, s71, -v146
	v_fmac_f32_e32 v146, 0x3377d1cf, v186
	v_fmac_f32_e32 v146, 0x3f317217, v186
	v_cmp_lt_f32_e64 vcc, |v186|, s72
	v_cndmask_b32_e64 v183, 0, v201, s[0:1]
	s_nop 0
	v_cndmask_b32_e32 v146, v186, v146, vcc
	v_sub_f32_e32 v183, v146, v183

.LBB0_356:
	v_or_b32_e32 v190, 48, v168
	v_ashrrev_i32_e32 v191, 31, v190
	v_cvt_pk_bf16_f32 v186, v176, v177
	v_lshlrev_b64 v[176:177], 10, v[190:191]
	v_cvt_pk_bf16_f32 v187, v180, v181
	v_lshl_add_u64 v[176:177], v[184:185], 0, v[176:177]
	s_and_b64 vcc, exec, s[12:13]
	s_mov_b64 s[0:1], -1
	v_cvt_pk_bf16_f32 v188, v178, v179
	v_cvt_pk_bf16_f32 v189, v182, v183
	global_store_dwordx4 v[176:177], v[186:189], off
	s_cbranch_vccnz .LBB0_360
	s_and_b64 vcc, exec, s[10:11]
	v_mov_b32_e32 v187, v61
	v_mov_b32_e32 v186, v60
	v_mov_b32_e32 v181, v59
	v_mov_b32_e32 v180, v58
	v_mov_b32_e32 v183, v65
	v_mov_b32_e32 v182, v64
	v_mov_b32_e32 v179, v63
	v_mov_b32_e32 v178, v62
	s_cbranch_vccnz .LBB0_359
	v_mul_f32_e32 v146, 0xbfb8aa3b, v62
	v_exp_f32_e32 v146, v146
	v_mul_f32_e32 v178, 0xbfb8aa3b, v58
	v_exp_f32_e32 v178, v178
	v_sub_f32_e32 v179, 1.0, v134
	v_add_f32_e32 v146, 1.0, v146
	v_rcp_f32_e32 v146, v146
	v_add_f32_e32 v178, 1.0, v178
	v_rcp_f32_e32 v178, v178
	v_sub_f32_e32 v181, 1.0, v135
	v_fma_f32 v146, v146, v179, v134
	v_cmp_gt_f32_e32 vcc, s70, v146
	v_sub_f32_e32 v182, 1.0, v131
	v_sub_f32_e32 v183, 1.0, v136
	v_cndmask_b32_e64 v179, 0, 32, vcc
	v_ldexp_f32 v146, v146, v179
	v_log_f32_e32 v146, v146
	v_sub_f32_e32 v179, 1.0, v130
	v_fma_f32 v178, v178, v179, v130
	v_cmp_gt_f32_e64 s[0:1], s70, v178
	v_mul_f32_e32 v179, 0x3f317217, v146
	v_fma_f32 v179, v146, s71, -v179
	v_fmac_f32_e32 v179, 0x3377d1cf, v146
	v_fmac_f32_e32 v179, 0x3f317217, v146
	v_cmp_lt_f32_e64 s[14:15], |v146|, s72
	v_cndmask_b32_e64 v180, 0, 32, s[0:1]
	v_ldexp_f32 v178, v178, v180
	v_cndmask_b32_e64 v146, v146, v179, s[14:15]
	v_mul_f32_e32 v179, 0xbfb8aa3b, v63
	v_exp_f32_e32 v179, v179
	v_log_f32_e32 v180, v178
	v_cndmask_b32_e32 v178, 0, v201, vcc
	v_sub_f32_e32 v178, v146, v178
	v_add_f32_e32 v179, 1.0, v179
	v_rcp_f32_e32 v179, v179
	v_mul_f32_e32 v146, 0x3f317217, v180
	v_fma_f32 v146, v180, s71, -v146
	v_fmac_f32_e32 v146, 0x3377d1cf, v180
	v_fmac_f32_e32 v146, 0x3f317217, v180
	v_cmp_lt_f32_e64 vcc, |v180|, s72
	v_fma_f32 v179, v179, v181, v135
	v_sub_f32_e32 v186, 1.0, v132
	v_cndmask_b32_e32 v146, v180, v146, vcc
	v_cmp_gt_f32_e32 vcc, s70, v179
	v_cndmask_b32_e64 v180, 0, v201, s[0:1]
	v_sub_f32_e32 v180, v146, v180
	v_cndmask_b32_e64 v181, 0, 32, vcc
	v_ldexp_f32 v179, v179, v181
	v_mul_f32_e32 v181, 0xbfb8aa3b, v59
	v_exp_f32_e32 v181, v181
	v_log_f32_e32 v179, v179
	v_sub_f32_e32 v187, 1.0, v137
	v_add_f32_e32 v181, 1.0, v181
	v_rcp_f32_e32 v181, v181
	v_mul_f32_e32 v146, 0x3f317217, v179
	v_fma_f32 v146, v179, s71, -v146
	v_fmac_f32_e32 v146, 0x3377d1cf, v179
	v_fma_f32 v181, v181, v182, v131
	v_cmp_gt_f32_e64 s[0:1], s70, v181
	v_fmac_f32_e32 v146, 0x3f317217, v179
	v_cmp_lt_f32_e64 s[14:15], |v179|, s72
	v_cndmask_b32_e64 v182, 0, 32, s[0:1]
	v_ldexp_f32 v181, v181, v182
	v_mul_f32_e32 v182, 0xbfb8aa3b, v64
	v_exp_f32_e32 v182, v182
	v_log_f32_e32 v181, v181
	v_cndmask_b32_e64 v146, v179, v146, s[14:15]
	v_cndmask_b32_e32 v179, 0, v201, vcc
	v_add_f32_e32 v182, 1.0, v182
	v_rcp_f32_e32 v182, v182
	v_sub_f32_e32 v179, v146, v179
	v_mul_f32_e32 v146, 0x3f317217, v181
	v_fma_f32 v146, v181, s71, -v146
	v_fmac_f32_e32 v146, 0x3377d1cf, v181
	v_fmac_f32_e32 v146, 0x3f317217, v181
	v_cmp_lt_f32_e64 vcc, |v181|, s72
	v_fma_f32 v182, v182, v183, v136
	s_nop 0
	v_cndmask_b32_e32 v146, v181, v146, vcc
	v_cmp_gt_f32_e32 vcc, s70, v182
	v_cndmask_b32_e64 v181, 0, v201, s[0:1]
	v_sub_f32_e32 v181, v146, v181
	v_cndmask_b32_e64 v183, 0, 32, vcc
	v_ldexp_f32 v182, v182, v183
	v_mul_f32_e32 v183, 0xbfb8aa3b, v60
	v_exp_f32_e32 v183, v183
	v_log_f32_e32 v182, v182
	v_add_f32_e32 v183, 1.0, v183
	v_rcp_f32_e32 v183, v183
	v_mul_f32_e32 v146, 0x3f317217, v182
	v_fma_f32 v146, v182, s71, -v146
	v_fmac_f32_e32 v146, 0x3377d1cf, v182
	v_fma_f32 v183, v183, v186, v132
	v_cmp_gt_f32_e64 s[0:1], s70, v183
	v_fmac_f32_e32 v146, 0x3f317217, v182
	v_cmp_lt_f32_e64 s[14:15], |v182|, s72
	v_cndmask_b32_e64 v186, 0, 32, s[0:1]
	v_ldexp_f32 v183, v183, v186
	v_mul_f32_e32 v186, 0xbfb8aa3b, v65
	v_exp_f32_e32 v186, v186
	v_log_f32_e32 v183, v183
	v_cndmask_b32_e64 v146, v182, v146, s[14:15]
	v_cndmask_b32_e32 v182, 0, v201, vcc
	v_add_f32_e32 v186, 1.0, v186
	v_rcp_f32_e32 v186, v186
	v_sub_f32_e32 v182, v146, v182
	v_mul_f32_e32 v146, 0x3f317217, v183
	v_fma_f32 v146, v183, s71, -v146
	v_fmac_f32_e32 v146, 0x3377d1cf, v183
	v_fmac_f32_e32 v146, 0x3f317217, v183
	v_cmp_lt_f32_e64 vcc, |v183|, s72
	v_fma_f32 v186, v186, v187, v137
	s_nop 0
	v_cndmask_b32_e32 v146, v183, v146, vcc
	v_cmp_gt_f32_e32 vcc, s70, v186
	v_cndmask_b32_e64 v183, 0, v201, s[0:1]
	s_nop 0
	v_cndmask_b32_e64 v187, 0, 32, vcc
	v_ldexp_f32 v186, v186, v187
	v_log_f32_e32 v187, v186
	v_mul_f32_e32 v186, 0xbfb8aa3b, v61
	v_exp_f32_e32 v188, v186
	v_sub_f32_e32 v186, v146, v183
	v_mul_f32_e32 v146, 0x3f317217, v187
	v_fma_f32 v146, v187, s71, -v146
	v_add_f32_e32 v183, 1.0, v188
	v_rcp_f32_e32 v183, v183
	v_sub_f32_e32 v188, 1.0, v133
	v_fmac_f32_e32 v146, 0x3377d1cf, v187
	v_fmac_f32_e32 v146, 0x3f317217, v187
	v_fma_f32 v183, v183, v188, v133
	v_cmp_gt_f32_e64 s[0:1], s70, v183
	v_cmp_lt_f32_e64 s[14:15], |v187|, s72
	s_nop 0
	v_cndmask_b32_e64 v188, 0, 32, s[0:1]
	v_ldexp_f32 v183, v183, v188
	v_log_f32_e32 v188, v183
	v_cndmask_b32_e64 v146, v187, v146, s[14:15]
	v_cndmask_b32_e32 v183, 0, v201, vcc
	v_sub_f32_e32 v183, v146, v183
	v_mul_f32_e32 v146, 0x3f317217, v188
	v_fma_f32 v146, v188, s71, -v146
	v_fmac_f32_e32 v146, 0x3377d1cf, v188
	v_fmac_f32_e32 v146, 0x3f317217, v188
	v_cmp_lt_f32_e64 vcc, |v188|, s72
	v_cndmask_b32_e64 v187, 0, v201, s[0:1]
	s_nop 0
	v_cndmask_b32_e32 v146, v188, v146, vcc
	v_sub_f32_e32 v187, v146, v187

.LBB0_362:
	v_cvt_pk_bf16_f32 v188, v178, v179
	v_lshlrev_b64 v[178:179], 10, v[168:169]
	v_lshl_add_u64 v[178:179], v[184:185], 0, v[178:179]
	v_cvt_pk_bf16_f32 v189, v182, v183
	v_cvt_pk_bf16_f32 v190, v180, v181
	v_add_co_u32_e32 v180, vcc, 0x20000, v178
	s_mov_b64 s[0:1], -1
	s_nop 0
	v_addc_co_u32_e32 v181, vcc, 0, v179, vcc
	s_and_b64 vcc, exec, s[12:13]
	v_cvt_pk_bf16_f32 v191, v186, v187
	global_store_dwordx4 v[180:181], v[188:191], off
	s_cbranch_vccnz .LBB0_366
	s_and_b64 vcc, exec, s[10:11]
	v_mov_b32_e32 v189, v45
	v_mov_b32_e32 v188, v44
	v_mov_b32_e32 v183, v43
	v_mov_b32_e32 v182, v42
	v_mov_b32_e32 v187, v49
	v_mov_b32_e32 v186, v48
	v_mov_b32_e32 v181, v47
	v_mov_b32_e32 v180, v46
	s_cbranch_vccnz .LBB0_365
	v_mul_f32_e32 v146, 0xbfb8aa3b, v46
	v_exp_f32_e32 v146, v146
	v_mul_f32_e32 v180, 0xbfb8aa3b, v42
	v_exp_f32_e32 v180, v180
	v_sub_f32_e32 v181, 1.0, v134
	v_add_f32_e32 v146, 1.0, v146
	v_rcp_f32_e32 v146, v146
	v_add_f32_e32 v180, 1.0, v180
	v_rcp_f32_e32 v180, v180
	v_sub_f32_e32 v183, 1.0, v135
	v_fma_f32 v146, v146, v181, v134
	v_cmp_gt_f32_e32 vcc, s70, v146
	v_sub_f32_e32 v186, 1.0, v131
	v_sub_f32_e32 v187, 1.0, v136
	v_cndmask_b32_e64 v181, 0, 32, vcc
	v_ldexp_f32 v146, v146, v181
	v_log_f32_e32 v146, v146
	v_sub_f32_e32 v181, 1.0, v130
	v_fma_f32 v180, v180, v181, v130
	v_cmp_gt_f32_e64 s[0:1], s70, v180
	v_mul_f32_e32 v181, 0x3f317217, v146
	v_fma_f32 v181, v146, s71, -v181
	v_fmac_f32_e32 v181, 0x3377d1cf, v146
	v_fmac_f32_e32 v181, 0x3f317217, v146
	v_cmp_lt_f32_e64 s[14:15], |v146|, s72
	v_cndmask_b32_e64 v182, 0, 32, s[0:1]
	v_ldexp_f32 v180, v180, v182
	v_cndmask_b32_e64 v146, v146, v181, s[14:15]
	v_mul_f32_e32 v181, 0xbfb8aa3b, v47
	v_exp_f32_e32 v181, v181
	v_log_f32_e32 v182, v180
	v_cndmask_b32_e32 v180, 0, v201, vcc
	v_sub_f32_e32 v180, v146, v180
	v_add_f32_e32 v181, 1.0, v181
	v_rcp_f32_e32 v181, v181
	v_mul_f32_e32 v146, 0x3f317217, v182
	v_fma_f32 v146, v182, s71, -v146
	v_fmac_f32_e32 v146, 0x3377d1cf, v182
	v_fmac_f32_e32 v146, 0x3f317217, v182
	v_cmp_lt_f32_e64 vcc, |v182|, s72
	v_fma_f32 v181, v181, v183, v135
	v_sub_f32_e32 v188, 1.0, v132
	v_cndmask_b32_e32 v146, v182, v146, vcc
	v_cmp_gt_f32_e32 vcc, s70, v181
	v_cndmask_b32_e64 v182, 0, v201, s[0:1]
	v_sub_f32_e32 v182, v146, v182
	v_cndmask_b32_e64 v183, 0, 32, vcc
	v_ldexp_f32 v181, v181, v183
	v_mul_f32_e32 v183, 0xbfb8aa3b, v43
	v_exp_f32_e32 v183, v183
	v_log_f32_e32 v181, v181
	v_sub_f32_e32 v189, 1.0, v137
	v_add_f32_e32 v183, 1.0, v183
	v_rcp_f32_e32 v183, v183
	v_mul_f32_e32 v146, 0x3f317217, v181
	v_fma_f32 v146, v181, s71, -v146
	v_fmac_f32_e32 v146, 0x3377d1cf, v181
	v_fma_f32 v183, v183, v186, v131
	v_cmp_gt_f32_e64 s[0:1], s70, v183
	v_fmac_f32_e32 v146, 0x3f317217, v181
	v_cmp_lt_f32_e64 s[14:15], |v181|, s72
	v_cndmask_b32_e64 v186, 0, 32, s[0:1]
	v_ldexp_f32 v183, v183, v186
	v_mul_f32_e32 v186, 0xbfb8aa3b, v48
	v_exp_f32_e32 v186, v186
	v_log_f32_e32 v183, v183
	v_cndmask_b32_e64 v146, v181, v146, s[14:15]
	v_cndmask_b32_e32 v181, 0, v201, vcc
	v_add_f32_e32 v186, 1.0, v186
	v_rcp_f32_e32 v186, v186
	v_sub_f32_e32 v181, v146, v181
	v_mul_f32_e32 v146, 0x3f317217, v183
	v_fma_f32 v146, v183, s71, -v146
	v_fmac_f32_e32 v146, 0x3377d1cf, v183
	v_fmac_f32_e32 v146, 0x3f317217, v183
	v_cmp_lt_f32_e64 vcc, |v183|, s72
	v_fma_f32 v186, v186, v187, v136
	s_nop 0
	v_cndmask_b32_e32 v146, v183, v146, vcc
	v_cmp_gt_f32_e32 vcc, s70, v186
	v_cndmask_b32_e64 v183, 0, v201, s[0:1]
	v_sub_f32_e32 v183, v146, v183
	v_cndmask_b32_e64 v187, 0, 32, vcc
	v_ldexp_f32 v186, v186, v187
	v_mul_f32_e32 v187, 0xbfb8aa3b, v44
	v_exp_f32_e32 v187, v187
	v_log_f32_e32 v186, v186
	v_add_f32_e32 v187, 1.0, v187
	v_rcp_f32_e32 v187, v187
	v_mul_f32_e32 v146, 0x3f317217, v186
	v_fma_f32 v146, v186, s71, -v146
	v_fmac_f32_e32 v146, 0x3377d1cf, v186
	v_fma_f32 v187, v187, v188, v132
	v_cmp_gt_f32_e64 s[0:1], s70, v187
	v_fmac_f32_e32 v146, 0x3f317217, v186
	v_cmp_lt_f32_e64 s[14:15], |v186|, s72
	v_cndmask_b32_e64 v188, 0, 32, s[0:1]
	v_ldexp_f32 v187, v187, v188
	v_mul_f32_e32 v188, 0xbfb8aa3b, v49
	v_exp_f32_e32 v188, v188
	v_log_f32_e32 v187, v187
	v_cndmask_b32_e64 v146, v186, v146, s[14:15]
	v_cndmask_b32_e32 v186, 0, v201, vcc
	v_add_f32_e32 v188, 1.0, v188
	v_rcp_f32_e32 v188, v188
	v_sub_f32_e32 v186, v146, v186
	v_mul_f32_e32 v146, 0x3f317217, v187
	v_fma_f32 v146, v187, s71, -v146
	v_fmac_f32_e32 v146, 0x3377d1cf, v187
	v_fmac_f32_e32 v146, 0x3f317217, v187
	v_cmp_lt_f32_e64 vcc, |v187|, s72
	v_fma_f32 v188, v188, v189, v137
	s_nop 0
	v_cndmask_b32_e32 v146, v187, v146, vcc
	v_cmp_gt_f32_e32 vcc, s70, v188
	v_cndmask_b32_e64 v187, 0, v201, s[0:1]
	s_nop 0
	v_cndmask_b32_e64 v189, 0, 32, vcc
	v_ldexp_f32 v188, v188, v189
	v_log_f32_e32 v189, v188
	v_mul_f32_e32 v188, 0xbfb8aa3b, v45
	v_exp_f32_e32 v190, v188
	v_sub_f32_e32 v188, v146, v187
	v_mul_f32_e32 v146, 0x3f317217, v189
	v_fma_f32 v146, v189, s71, -v146
	v_add_f32_e32 v187, 1.0, v190
	v_rcp_f32_e32 v187, v187
	v_sub_f32_e32 v190, 1.0, v133
	v_fmac_f32_e32 v146, 0x3377d1cf, v189
	v_fmac_f32_e32 v146, 0x3f317217, v189
	v_fma_f32 v187, v187, v190, v133
	v_cmp_gt_f32_e64 s[0:1], s70, v187
	v_cmp_lt_f32_e64 s[14:15], |v189|, s72
	s_nop 0
	v_cndmask_b32_e64 v190, 0, 32, s[0:1]
	v_ldexp_f32 v187, v187, v190
	v_log_f32_e32 v190, v187
	v_cndmask_b32_e64 v146, v189, v146, s[14:15]
	v_cndmask_b32_e32 v187, 0, v201, vcc
	v_sub_f32_e32 v187, v146, v187
	v_mul_f32_e32 v146, 0x3f317217, v190
	v_fma_f32 v146, v190, s71, -v146
	v_fmac_f32_e32 v146, 0x3377d1cf, v190
	v_fmac_f32_e32 v146, 0x3f317217, v190
	v_cmp_lt_f32_e64 vcc, |v190|, s72
	v_cndmask_b32_e64 v189, 0, v201, s[0:1]
	s_nop 0
	v_cndmask_b32_e32 v146, v190, v146, vcc
	v_sub_f32_e32 v189, v146, v189

.LBB0_368:
	v_cvt_pk_bf16_f32 v190, v180, v181
	v_lshlrev_b64 v[180:181], 10, v[168:169]
	v_lshl_add_u64 v[180:181], v[184:185], 0, v[180:181]
	v_cvt_pk_bf16_f32 v191, v186, v187
	v_cvt_pk_bf16_f32 v192, v182, v183
	v_add_co_u32_e32 v182, vcc, 0x24000, v180
	s_mov_b64 s[0:1], -1
	s_nop 0
	v_addc_co_u32_e32 v183, vcc, 0, v181, vcc
	s_and_b64 vcc, exec, s[12:13]
	v_cvt_pk_bf16_f32 v193, v188, v189
	global_store_dwordx4 v[182:183], v[190:193], off
	s_cbranch_vccnz .LBB0_372
	s_and_b64 vcc, exec, s[10:11]
	v_mov_b32_e32 v191, v29
	v_mov_b32_e32 v190, v28
	v_mov_b32_e32 v187, v27
	v_mov_b32_e32 v186, v26
	v_mov_b32_e32 v189, v33
	v_mov_b32_e32 v188, v32
	v_mov_b32_e32 v183, v31
	v_mov_b32_e32 v182, v30
	s_cbranch_vccnz .LBB0_371
	v_mul_f32_e32 v146, 0xbfb8aa3b, v30
	v_exp_f32_e32 v146, v146
	v_mul_f32_e32 v182, 0xbfb8aa3b, v26
	v_exp_f32_e32 v182, v182
	v_sub_f32_e32 v183, 1.0, v134
	v_add_f32_e32 v146, 1.0, v146
	v_rcp_f32_e32 v146, v146
	v_add_f32_e32 v182, 1.0, v182
	v_rcp_f32_e32 v182, v182
	v_sub_f32_e32 v187, 1.0, v135
	v_fma_f32 v146, v146, v183, v134
	v_cmp_gt_f32_e32 vcc, s70, v146
	v_sub_f32_e32 v188, 1.0, v131
	v_sub_f32_e32 v189, 1.0, v136
	v_cndmask_b32_e64 v183, 0, 32, vcc
	v_ldexp_f32 v146, v146, v183
	v_log_f32_e32 v146, v146
	v_sub_f32_e32 v183, 1.0, v130
	v_fma_f32 v182, v182, v183, v130
	v_cmp_gt_f32_e64 s[0:1], s70, v182
	v_mul_f32_e32 v183, 0x3f317217, v146
	v_fma_f32 v183, v146, s71, -v183
	v_fmac_f32_e32 v183, 0x3377d1cf, v146
	v_fmac_f32_e32 v183, 0x3f317217, v146
	v_cmp_lt_f32_e64 s[14:15], |v146|, s72
	v_cndmask_b32_e64 v186, 0, 32, s[0:1]
	v_ldexp_f32 v182, v182, v186
	v_cndmask_b32_e64 v146, v146, v183, s[14:15]
	v_mul_f32_e32 v183, 0xbfb8aa3b, v31
	v_exp_f32_e32 v183, v183
	v_log_f32_e32 v186, v182
	v_cndmask_b32_e32 v182, 0, v201, vcc
	v_sub_f32_e32 v182, v146, v182
	v_add_f32_e32 v183, 1.0, v183
	v_rcp_f32_e32 v183, v183
	v_mul_f32_e32 v146, 0x3f317217, v186
	v_fma_f32 v146, v186, s71, -v146
	v_fmac_f32_e32 v146, 0x3377d1cf, v186
	v_fmac_f32_e32 v146, 0x3f317217, v186
	v_cmp_lt_f32_e64 vcc, |v186|, s72
	v_fma_f32 v183, v183, v187, v135
	v_sub_f32_e32 v190, 1.0, v132
	v_cndmask_b32_e32 v146, v186, v146, vcc
	v_cmp_gt_f32_e32 vcc, s70, v183
	v_cndmask_b32_e64 v186, 0, v201, s[0:1]
	v_sub_f32_e32 v186, v146, v186
	v_cndmask_b32_e64 v187, 0, 32, vcc
	v_ldexp_f32 v183, v183, v187
	v_mul_f32_e32 v187, 0xbfb8aa3b, v27
	v_exp_f32_e32 v187, v187
	v_log_f32_e32 v183, v183
	v_sub_f32_e32 v191, 1.0, v137
	v_add_f32_e32 v187, 1.0, v187
	v_rcp_f32_e32 v187, v187
	v_mul_f32_e32 v146, 0x3f317217, v183
	v_fma_f32 v146, v183, s71, -v146
	v_fmac_f32_e32 v146, 0x3377d1cf, v183
	v_fma_f32 v187, v187, v188, v131
	v_cmp_gt_f32_e64 s[0:1], s70, v187
	v_fmac_f32_e32 v146, 0x3f317217, v183
	v_cmp_lt_f32_e64 s[14:15], |v183|, s72
	v_cndmask_b32_e64 v188, 0, 32, s[0:1]
	v_ldexp_f32 v187, v187, v188
	v_mul_f32_e32 v188, 0xbfb8aa3b, v32
	v_exp_f32_e32 v188, v188
	v_log_f32_e32 v187, v187
	v_cndmask_b32_e64 v146, v183, v146, s[14:15]
	v_cndmask_b32_e32 v183, 0, v201, vcc
	v_add_f32_e32 v188, 1.0, v188
	v_rcp_f32_e32 v188, v188
	v_sub_f32_e32 v183, v146, v183
	v_mul_f32_e32 v146, 0x3f317217, v187
	v_fma_f32 v146, v187, s71, -v146
	v_fmac_f32_e32 v146, 0x3377d1cf, v187
	v_fmac_f32_e32 v146, 0x3f317217, v187
	v_cmp_lt_f32_e64 vcc, |v187|, s72
	v_fma_f32 v188, v188, v189, v136
	s_nop 0
	v_cndmask_b32_e32 v146, v187, v146, vcc
	v_cmp_gt_f32_e32 vcc, s70, v188
	v_cndmask_b32_e64 v187, 0, v201, s[0:1]
	v_sub_f32_e32 v187, v146, v187
	v_cndmask_b32_e64 v189, 0, 32, vcc
	v_ldexp_f32 v188, v188, v189
	v_mul_f32_e32 v189, 0xbfb8aa3b, v28
	v_exp_f32_e32 v189, v189
	v_log_f32_e32 v188, v188
	v_add_f32_e32 v189, 1.0, v189
	v_rcp_f32_e32 v189, v189
	v_mul_f32_e32 v146, 0x3f317217, v188
	v_fma_f32 v146, v188, s71, -v146
	v_fmac_f32_e32 v146, 0x3377d1cf, v188
	v_fma_f32 v189, v189, v190, v132
	v_cmp_gt_f32_e64 s[0:1], s70, v189
	v_fmac_f32_e32 v146, 0x3f317217, v188
	v_cmp_lt_f32_e64 s[14:15], |v188|, s72
	v_cndmask_b32_e64 v190, 0, 32, s[0:1]
	v_ldexp_f32 v189, v189, v190
	v_mul_f32_e32 v190, 0xbfb8aa3b, v33
	v_exp_f32_e32 v190, v190
	v_log_f32_e32 v189, v189
	v_cndmask_b32_e64 v146, v188, v146, s[14:15]
	v_cndmask_b32_e32 v188, 0, v201, vcc
	v_add_f32_e32 v190, 1.0, v190
	v_rcp_f32_e32 v190, v190
	v_sub_f32_e32 v188, v146, v188
	v_mul_f32_e32 v146, 0x3f317217, v189
	v_fma_f32 v146, v189, s71, -v146
	v_fmac_f32_e32 v146, 0x3377d1cf, v189
	v_fmac_f32_e32 v146, 0x3f317217, v189
	v_cmp_lt_f32_e64 vcc, |v189|, s72
	v_fma_f32 v190, v190, v191, v137
	s_nop 0
	v_cndmask_b32_e32 v146, v189, v146, vcc
	v_cmp_gt_f32_e32 vcc, s70, v190
	v_cndmask_b32_e64 v189, 0, v201, s[0:1]
	s_nop 0
	v_cndmask_b32_e64 v191, 0, 32, vcc
	v_ldexp_f32 v190, v190, v191
	v_log_f32_e32 v191, v190
	v_mul_f32_e32 v190, 0xbfb8aa3b, v29
	v_exp_f32_e32 v192, v190
	v_sub_f32_e32 v190, v146, v189
	v_mul_f32_e32 v146, 0x3f317217, v191
	v_fma_f32 v146, v191, s71, -v146
	v_add_f32_e32 v189, 1.0, v192
	v_rcp_f32_e32 v189, v189
	v_sub_f32_e32 v192, 1.0, v133
	v_fmac_f32_e32 v146, 0x3377d1cf, v191
	v_fmac_f32_e32 v146, 0x3f317217, v191
	v_fma_f32 v189, v189, v192, v133
	v_cmp_gt_f32_e64 s[0:1], s70, v189
	v_cmp_lt_f32_e64 s[14:15], |v191|, s72
	s_nop 0
	v_cndmask_b32_e64 v192, 0, 32, s[0:1]
	v_ldexp_f32 v189, v189, v192
	v_log_f32_e32 v192, v189
	v_cndmask_b32_e64 v146, v191, v146, s[14:15]
	v_cndmask_b32_e32 v189, 0, v201, vcc
	v_sub_f32_e32 v189, v146, v189
	v_mul_f32_e32 v146, 0x3f317217, v192
	v_fma_f32 v146, v192, s71, -v146
	v_fmac_f32_e32 v146, 0x3377d1cf, v192
	v_fmac_f32_e32 v146, 0x3f317217, v192
	v_cmp_lt_f32_e64 vcc, |v192|, s72
	v_cndmask_b32_e64 v191, 0, v201, s[0:1]
	s_nop 0
	v_cndmask_b32_e32 v146, v192, v146, vcc
	v_sub_f32_e32 v191, v146, v191

.LBB0_374:
	v_cvt_pk_bf16_f32 v204, v182, v183
	v_lshlrev_b64 v[182:183], 10, v[168:169]
	v_lshl_add_u64 v[182:183], v[184:185], 0, v[182:183]
	v_cvt_pk_bf16_f32 v205, v188, v189
	v_cvt_pk_bf16_f32 v206, v186, v187
	v_add_co_u32_e32 v186, vcc, 0x28000, v182
	s_mov_b64 s[0:1], -1
	s_nop 0
	v_addc_co_u32_e32 v187, vcc, 0, v183, vcc
	s_and_b64 vcc, exec, s[12:13]
	v_cvt_pk_bf16_f32 v207, v190, v191
	global_store_dwordx4 v[186:187], v[204:207], off
	s_cbranch_vccnz .LBB0_378
	s_and_b64 vcc, exec, s[10:11]
	v_mov_b32_e32 v193, v13
	v_mov_b32_e32 v192, v12
	v_mov_b32_e32 v189, v11
	v_mov_b32_e32 v188, v10
	v_mov_b32_e32 v191, v17
	v_mov_b32_e32 v190, v16
	v_mov_b32_e32 v187, v15
	v_mov_b32_e32 v186, v14
	s_cbranch_vccnz .LBB0_377
	v_mul_f32_e32 v146, 0xbfb8aa3b, v14
	v_exp_f32_e32 v146, v146
	v_mul_f32_e32 v186, 0xbfb8aa3b, v10
	v_exp_f32_e32 v186, v186
	v_sub_f32_e32 v187, 1.0, v134
	v_add_f32_e32 v146, 1.0, v146
	v_rcp_f32_e32 v146, v146
	v_add_f32_e32 v186, 1.0, v186
	v_rcp_f32_e32 v186, v186
	v_fmac_f32_e32 v134, v146, v187
	v_cmp_gt_f32_e32 vcc, s70, v134
	v_sub_f32_e32 v187, 1.0, v135
	s_nop 0
	v_cndmask_b32_e64 v146, 0, 32, vcc
	v_ldexp_f32 v134, v134, v146
	v_log_f32_e32 v134, v134
	v_sub_f32_e32 v146, 1.0, v130
	v_fmac_f32_e32 v130, v186, v146
	v_cmp_gt_f32_e64 s[0:1], s70, v130
	v_mul_f32_e32 v146, 0x3f317217, v134
	v_fma_f32 v146, v134, s71, -v146
	v_fmac_f32_e32 v146, 0x3377d1cf, v134
	v_fmac_f32_e32 v146, 0x3f317217, v134
	v_cmp_lt_f32_e64 s[14:15], |v134|, s72
	v_cndmask_b32_e64 v186, 0, 32, s[0:1]
	v_ldexp_f32 v130, v130, v186
	v_cndmask_b32_e64 v134, v134, v146, s[14:15]
	v_cndmask_b32_e32 v146, 0, v201, vcc
	v_sub_f32_e32 v186, v134, v146
	v_mul_f32_e32 v146, 0xbfb8aa3b, v15
	v_exp_f32_e32 v146, v146
	v_log_f32_e32 v130, v130
	v_add_f32_e32 v146, 1.0, v146
	v_rcp_f32_e32 v146, v146
	v_mul_f32_e32 v134, 0x3f317217, v130
	v_fma_f32 v134, v130, s71, -v134
	v_fmac_f32_e32 v134, 0x3377d1cf, v130
	v_fmac_f32_e32 v134, 0x3f317217, v130
	v_cmp_lt_f32_e64 vcc, |v130|, s72
	v_fmac_f32_e32 v135, v146, v187
	s_nop 0
	v_cndmask_b32_e32 v130, v130, v134, vcc
	v_cmp_gt_f32_e32 vcc, s70, v135
	v_cndmask_b32_e64 v134, 0, v201, s[0:1]
	v_sub_f32_e32 v188, v130, v134
	v_cndmask_b32_e64 v146, 0, 32, vcc
	v_ldexp_f32 v135, v135, v146
	v_mul_f32_e32 v146, 0xbfb8aa3b, v11
	v_exp_f32_e32 v146, v146
	v_log_f32_e32 v135, v135
	v_add_f32_e32 v134, 1.0, v146
	v_rcp_f32_e32 v134, v134
	v_mul_f32_e32 v130, 0x3f317217, v135
	v_sub_f32_e32 v146, 1.0, v131
	v_fma_f32 v130, v135, s71, -v130
	v_fmac_f32_e32 v131, v134, v146
	v_fmac_f32_e32 v130, 0x3377d1cf, v135
	v_cmp_gt_f32_e64 s[0:1], s70, v131
	v_fmac_f32_e32 v130, 0x3f317217, v135
	v_cmp_lt_f32_e64 s[14:15], |v135|, s72
	v_cndmask_b32_e64 v134, 0, 32, s[0:1]
	v_ldexp_f32 v131, v131, v134
	v_cndmask_b32_e64 v130, v135, v130, s[14:15]
	v_cndmask_b32_e32 v134, 0, v201, vcc
	v_sub_f32_e32 v187, v130, v134
	v_mul_f32_e32 v134, 0xbfb8aa3b, v16
	v_exp_f32_e32 v134, v134
	v_log_f32_e32 v131, v131
	v_sub_f32_e32 v135, 1.0, v136
	v_add_f32_e32 v134, 1.0, v134
	v_rcp_f32_e32 v134, v134
	v_mul_f32_e32 v130, 0x3f317217, v131
	v_fma_f32 v130, v131, s71, -v130
	v_fmac_f32_e32 v130, 0x3377d1cf, v131
	v_fmac_f32_e32 v136, v134, v135
	v_mul_f32_e32 v135, 0xbfb8aa3b, v12
	v_fmac_f32_e32 v130, 0x3f317217, v131
	v_cmp_lt_f32_e64 vcc, |v131|, s72
	v_exp_f32_e32 v135, v135
	s_nop 0
	v_cndmask_b32_e32 v130, v131, v130, vcc
	v_cmp_gt_f32_e32 vcc, s70, v136
	v_cndmask_b32_e64 v131, 0, v201, s[0:1]
	v_sub_f32_e32 v189, v130, v131
	v_cndmask_b32_e64 v134, 0, 32, vcc
	v_ldexp_f32 v134, v136, v134
	v_log_f32_e32 v134, v134
	v_add_f32_e32 v131, 1.0, v135
	v_rcp_f32_e32 v131, v131
	v_sub_f32_e32 v135, 1.0, v132
	v_mul_f32_e32 v130, 0x3f317217, v134
	v_fma_f32 v130, v134, s71, -v130
	v_fmac_f32_e32 v132, v131, v135
	v_fmac_f32_e32 v130, 0x3377d1cf, v134
	v_cmp_gt_f32_e64 s[0:1], s70, v132
	v_fmac_f32_e32 v130, 0x3f317217, v134
	v_cmp_lt_f32_e64 s[14:15], |v134|, s72
	v_cndmask_b32_e64 v131, 0, 32, s[0:1]
	v_ldexp_f32 v131, v132, v131
	v_cndmask_b32_e64 v130, v134, v130, s[14:15]
	v_cndmask_b32_e32 v132, 0, v201, vcc
	v_sub_f32_e32 v190, v130, v132
	v_mul_f32_e32 v132, 0xbfb8aa3b, v17
	v_exp_f32_e32 v132, v132
	v_log_f32_e32 v131, v131
	v_sub_f32_e32 v134, 1.0, v137
	v_add_f32_e32 v132, 1.0, v132
	v_rcp_f32_e32 v132, v132
	v_mul_f32_e32 v130, 0x3f317217, v131
	v_fma_f32 v130, v131, s71, -v130
	v_fmac_f32_e32 v130, 0x3377d1cf, v131
	v_fmac_f32_e32 v137, v132, v134
	v_mul_f32_e32 v134, 0xbfb8aa3b, v13
	v_exp_f32_e32 v134, v134
	v_fmac_f32_e32 v130, 0x3f317217, v131
	v_cmp_lt_f32_e64 vcc, |v131|, s72
	s_nop 1
	v_cndmask_b32_e32 v130, v131, v130, vcc
	v_cndmask_b32_e64 v131, 0, v201, s[0:1]
	v_sub_f32_e32 v192, v130, v131
	v_add_f32_e32 v131, 1.0, v134
	v_cmp_gt_f32_e32 vcc, s70, v137
	v_rcp_f32_e32 v131, v131
	v_sub_f32_e32 v134, 1.0, v133
	v_cndmask_b32_e64 v132, 0, 32, vcc
	v_ldexp_f32 v132, v137, v132
	v_log_f32_e32 v132, v132
	v_fmac_f32_e32 v133, v131, v134
	v_cmp_gt_f32_e64 s[0:1], s70, v133
	v_mul_f32_e32 v130, 0x3f317217, v132
	s_nop 0
	v_cndmask_b32_e64 v131, 0, 32, s[0:1]
	v_ldexp_f32 v131, v133, v131
	v_fma_f32 v130, v132, s71, -v130
	v_log_f32_e32 v131, v131
	v_fmac_f32_e32 v130, 0x3377d1cf, v132
	v_fmac_f32_e32 v130, 0x3f317217, v132
	v_cmp_lt_f32_e64 s[14:15], |v132|, s72
	s_nop 1
	v_cndmask_b32_e64 v130, v132, v130, s[14:15]
	v_cndmask_b32_e32 v132, 0, v201, vcc
	v_sub_f32_e32 v191, v130, v132
	v_mul_f32_e32 v130, 0x3f317217, v131
	v_fma_f32 v130, v131, s71, -v130
	v_fmac_f32_e32 v130, 0x3377d1cf, v131
	v_fmac_f32_e32 v130, 0x3f317217, v131
	v_cmp_lt_f32_e64 vcc, |v131|, s72
	s_nop 1
	v_cndmask_b32_e32 v130, v131, v130, vcc
	v_cndmask_b32_e64 v131, 0, v201, s[0:1]
	v_sub_f32_e32 v193, v130, v131

.LBB0_380:
	v_lshlrev_b64 v[134:135], 10, v[168:169]
	v_lshl_add_u64 v[184:185], v[184:185], 0, v[134:135]
	v_add_co_u32_e32 v134, vcc, 0x2c000, v184
	v_cvt_pk_bf16_f32 v130, v186, v187
	v_cvt_pk_bf16_f32 v131, v190, v191
	v_cvt_pk_bf16_f32 v132, v188, v189
	v_cvt_pk_bf16_f32 v133, v192, v193
	s_nop 1
	v_addc_co_u32_e32 v135, vcc, 0, v185, vcc
	global_store_dwordx4 v[134:135], v[130:133], off
	v_mov_b32_e32 v134, 0
	s_and_b64 vcc, exec, s[10:11]
	v_mov_b32_e32 v135, 0
	v_mov_b32_e32 v136, 0
	v_mov_b32_e32 v137, 0
	v_mov_b32_e32 v130, 0
	v_mov_b32_e32 v131, 0
	v_mov_b32_e32 v132, 0
	v_mov_b32_e32 v133, 0
	s_cbranch_vccnz .LBB0_382
	global_load_dwordx4 v[134:137], v203, s[20:21] offset:512
	global_load_dwordx4 v[130:133], v203, s[20:21] offset:528

.LBB0_508:
	v_lshl_add_u32 v146, s28, 8, v1
	v_ashrrev_i32_e32 v147, 31, v146
	v_lshl_add_u64 v[144:145], v[146:147], 4, s[8:9]
	global_load_dwordx4 v[156:159], v[144:145], off
	global_load_dwordx4 v[206:209], v[144:145], off offset:256
	global_load_dwordx4 v[210:213], v[144:145], off offset:512
	global_load_dwordx4 v[214:217], v[144:145], off offset:768
	global_load_dwordx4 v[218:221], v[144:145], off offset:2048
	global_load_dwordx4 v[222:225], v[144:145], off offset:2304
	global_load_dwordx4 v[226:229], v[144:145], off offset:2560
	global_load_dwordx4 v[230:233], v[144:145], off offset:2816
	s_lshl_b32 s21, s52, 8
	s_and_b32 s21, s21, 0x100
	s_cmp_lt_i32 s52, 2
	s_cselect_b64 vcc, -1, 0
	s_and_b64 s[30:31], vcc, exec
	v_or_b32_e32 v138, s21, v149
	s_cselect_b32 s21, 0, 0x4000000
	s_add_u32 s30, s45, s21
	v_lshlrev_b64 v[162:163], 10, v[146:147]
	v_cndmask_b32_e32 v147, 1.0, v154, vcc
	v_lshlrev_b32_e32 v138, 1, v138
	s_addc_u32 s31, s46, 0
	v_or_b32_e32 v160, 16, v146
	v_ashrrev_i32_e32 v161, 31, v160
	v_lshl_add_u64 v[164:165], v[160:161], 4, s[8:9]
	s_andn2_b64 vcc, exec, s[6:7]
	s_mov_b64 s[6:7], -1
	s_waitcnt vmcnt(0)
	v_mov_b32_e32 v144, v157
	v_mov_b32_e32 v145, v158
	v_mov_b32_e32 v157, v159
	v_pk_add_f32 v[144:145], v[144:145], v[156:157]
	s_nop 0
	v_add_f32_e32 v144, v144, v145
	v_fmamk_f32 v144, v144, 0x3b800000, v153
	v_rsq_f32_e32 v155, v144
	v_lshl_add_u64 v[144:145], s[30:31], 0, v[138:139]
	v_lshl_add_u64 v[156:157], v[144:145], 0, v[162:163]
	v_mul_f32_e32 v138, v147, v155
	v_pk_mul_f32 v[116:117], v[116:117], v[138:139] op_sel_hi:[1,0]
	v_pk_mul_f32 v[114:115], v[114:115], v[138:139] op_sel_hi:[1,0]
	v_pk_mul_f32 v[120:121], v[120:121], v[138:139] op_sel_hi:[1,0]
	v_pk_mul_f32 v[118:119], v[118:119], v[138:139] op_sel_hi:[1,0]
	v_cvt_pk_bf16_f32 v114, v114, v115
	v_cvt_pk_bf16_f32 v115, v116, v117
	v_pk_mul_f32 v[124:125], v[124:125], v[138:139] op_sel_hi:[1,0]
	v_cvt_pk_bf16_f32 v116, v118, v119
	v_cvt_pk_bf16_f32 v117, v120, v121
	v_pk_mul_f32 v[122:123], v[122:123], v[138:139] op_sel_hi:[1,0]
	v_pk_mul_f32 v[128:129], v[128:129], v[138:139] op_sel_hi:[1,0]
	v_pk_mul_f32 v[126:127], v[126:127], v[138:139] op_sel_hi:[1,0]
	global_store_dwordx4 v[156:157], v[114:117], off
	v_or_b32_e32 v118, 32, v146
	v_ashrrev_i32_e32 v119, 31, v118
	v_cvt_pk_bf16_f32 v114, v122, v123
	v_cvt_pk_bf16_f32 v115, v124, v125
	v_cvt_pk_bf16_f32 v116, v126, v127
	v_cvt_pk_bf16_f32 v117, v128, v129
	global_store_dwordx4 v[156:157], v[114:117], off offset:256
	s_nop 1
	v_mov_b64_e32 v[114:115], v[206:207]
	v_mov_b64_e32 v[116:117], v[208:209]
	v_mov_b32_e32 v120, v115
	v_mov_b32_e32 v121, v116
	v_mov_b32_e32 v115, v117
	v_pk_add_f32 v[114:115], v[120:121], v[114:115]
	v_lshl_add_u64 v[116:117], v[118:119], 4, s[8:9]
	v_add_f32_e32 v114, v114, v115
	v_fmamk_f32 v114, v114, 0x3b800000, v153
	v_rsq_f32_e32 v120, v114
	v_lshlrev_b64 v[114:115], 10, v[160:161]
	v_lshl_add_u64 v[114:115], v[144:145], 0, v[114:115]
	v_mul_f32_e32 v120, v147, v120
	v_pk_mul_f32 v[100:101], v[100:101], v[120:121] op_sel_hi:[1,0]
	v_pk_mul_f32 v[98:99], v[98:99], v[120:121] op_sel_hi:[1,0]
	v_pk_mul_f32 v[104:105], v[104:105], v[120:121] op_sel_hi:[1,0]
	v_pk_mul_f32 v[102:103], v[102:103], v[120:121] op_sel_hi:[1,0]
	v_cvt_pk_bf16_f32 v98, v98, v99
	v_cvt_pk_bf16_f32 v99, v100, v101
	v_pk_mul_f32 v[108:109], v[108:109], v[120:121] op_sel_hi:[1,0]
	v_cvt_pk_bf16_f32 v100, v102, v103
	v_cvt_pk_bf16_f32 v101, v104, v105
	v_pk_mul_f32 v[106:107], v[106:107], v[120:121] op_sel_hi:[1,0]
	v_pk_mul_f32 v[112:113], v[112:113], v[120:121] op_sel_hi:[1,0]
	v_pk_mul_f32 v[110:111], v[110:111], v[120:121] op_sel_hi:[1,0]
	global_store_dwordx4 v[114:115], v[98:101], off
	v_or_b32_e32 v102, 48, v146
	v_ashrrev_i32_e32 v103, 31, v102
	v_cvt_pk_bf16_f32 v98, v106, v107
	v_cvt_pk_bf16_f32 v99, v108, v109
	v_cvt_pk_bf16_f32 v100, v110, v111
	v_cvt_pk_bf16_f32 v101, v112, v113
	global_store_dwordx4 v[114:115], v[98:101], off offset:256
	s_nop 1
	v_mov_b64_e32 v[98:99], v[210:211]
	v_mov_b64_e32 v[100:101], v[212:213]
	v_mov_b32_e32 v104, v99
	v_mov_b32_e32 v105, v100
	v_mov_b32_e32 v99, v101
	v_pk_add_f32 v[98:99], v[104:105], v[98:99]
	v_lshl_add_u64 v[100:101], v[102:103], 4, s[8:9]
	v_add_f32_e32 v98, v98, v99
	v_fmamk_f32 v98, v98, 0x3b800000, v153
	v_rsq_f32_e32 v104, v98
	v_lshlrev_b64 v[98:99], 10, v[118:119]
	v_lshl_add_u64 v[98:99], v[144:145], 0, v[98:99]
	v_mul_f32_e32 v104, v147, v104
	v_pk_mul_f32 v[84:85], v[84:85], v[104:105] op_sel_hi:[1,0]
	v_pk_mul_f32 v[82:83], v[82:83], v[104:105] op_sel_hi:[1,0]
	v_pk_mul_f32 v[88:89], v[88:89], v[104:105] op_sel_hi:[1,0]
	v_pk_mul_f32 v[86:87], v[86:87], v[104:105] op_sel_hi:[1,0]
	v_cvt_pk_bf16_f32 v82, v82, v83
	v_cvt_pk_bf16_f32 v83, v84, v85
	v_pk_mul_f32 v[92:93], v[92:93], v[104:105] op_sel_hi:[1,0]
	v_cvt_pk_bf16_f32 v84, v86, v87
	v_cvt_pk_bf16_f32 v85, v88, v89
	v_pk_mul_f32 v[90:91], v[90:91], v[104:105] op_sel_hi:[1,0]
	v_pk_mul_f32 v[96:97], v[96:97], v[104:105] op_sel_hi:[1,0]
	v_pk_mul_f32 v[94:95], v[94:95], v[104:105] op_sel_hi:[1,0]
	global_store_dwordx4 v[98:99], v[82:85], off
	v_add_u32_e32 v86, 0x80, v146
	v_ashrrev_i32_e32 v87, 31, v86
	v_cvt_pk_bf16_f32 v82, v90, v91
	v_cvt_pk_bf16_f32 v83, v92, v93
	v_cvt_pk_bf16_f32 v84, v94, v95
	v_cvt_pk_bf16_f32 v85, v96, v97
	global_store_dwordx4 v[98:99], v[82:85], off offset:256
	s_nop 1
	v_mov_b64_e32 v[82:83], v[214:215]
	v_mov_b64_e32 v[84:85], v[216:217]
	v_mov_b32_e32 v88, v83
	v_mov_b32_e32 v89, v84
	v_mov_b32_e32 v83, v85
	v_pk_add_f32 v[82:83], v[88:89], v[82:83]
	v_lshl_add_u64 v[84:85], v[86:87], 4, s[8:9]
	v_add_f32_e32 v82, v82, v83
	v_fmamk_f32 v82, v82, 0x3b800000, v153
	v_rsq_f32_e32 v88, v82
	v_lshlrev_b64 v[82:83], 10, v[102:103]
	v_lshl_add_u64 v[82:83], v[144:145], 0, v[82:83]
	v_mul_f32_e32 v88, v147, v88
	v_pk_mul_f32 v[68:69], v[68:69], v[88:89] op_sel_hi:[1,0]
	v_pk_mul_f32 v[66:67], v[66:67], v[88:89] op_sel_hi:[1,0]
	v_pk_mul_f32 v[72:73], v[72:73], v[88:89] op_sel_hi:[1,0]
	v_pk_mul_f32 v[70:71], v[70:71], v[88:89] op_sel_hi:[1,0]
	v_cvt_pk_bf16_f32 v66, v66, v67
	v_cvt_pk_bf16_f32 v67, v68, v69
	v_pk_mul_f32 v[76:77], v[76:77], v[88:89] op_sel_hi:[1,0]
	v_cvt_pk_bf16_f32 v68, v70, v71
	v_cvt_pk_bf16_f32 v69, v72, v73
	v_pk_mul_f32 v[74:75], v[74:75], v[88:89] op_sel_hi:[1,0]
	v_pk_mul_f32 v[80:81], v[80:81], v[88:89] op_sel_hi:[1,0]
	v_pk_mul_f32 v[78:79], v[78:79], v[88:89] op_sel_hi:[1,0]
	global_store_dwordx4 v[82:83], v[66:69], off
	v_add_u32_e32 v70, 0x90, v146
	v_ashrrev_i32_e32 v71, 31, v70
	v_cvt_pk_bf16_f32 v66, v74, v75
	v_cvt_pk_bf16_f32 v67, v76, v77
	v_cvt_pk_bf16_f32 v68, v78, v79
	v_cvt_pk_bf16_f32 v69, v80, v81
	global_store_dwordx4 v[82:83], v[66:69], off offset:256
	s_nop 1
	v_mov_b64_e32 v[66:67], v[218:219]
	v_mov_b64_e32 v[68:69], v[220:221]
	v_mov_b32_e32 v72, v67
	v_mov_b32_e32 v73, v68
	v_mov_b32_e32 v67, v69
	v_pk_add_f32 v[66:67], v[72:73], v[66:67]
	v_lshl_add_u64 v[68:69], v[70:71], 4, s[8:9]
	v_add_f32_e32 v66, v66, v67
	v_fmamk_f32 v66, v66, 0x3b800000, v153
	v_rsq_f32_e32 v72, v66
	v_lshlrev_b64 v[66:67], 10, v[86:87]
	v_lshl_add_u64 v[66:67], v[144:145], 0, v[66:67]
	v_mul_f32_e32 v72, v147, v72
	v_pk_mul_f32 v[52:53], v[52:53], v[72:73] op_sel_hi:[1,0]
	v_pk_mul_f32 v[50:51], v[50:51], v[72:73] op_sel_hi:[1,0]
	v_pk_mul_f32 v[56:57], v[56:57], v[72:73] op_sel_hi:[1,0]
	v_pk_mul_f32 v[54:55], v[54:55], v[72:73] op_sel_hi:[1,0]
	v_cvt_pk_bf16_f32 v50, v50, v51
	v_cvt_pk_bf16_f32 v51, v52, v53
	v_pk_mul_f32 v[60:61], v[60:61], v[72:73] op_sel_hi:[1,0]
	v_cvt_pk_bf16_f32 v52, v54, v55
	v_cvt_pk_bf16_f32 v53, v56, v57
	v_pk_mul_f32 v[58:59], v[58:59], v[72:73] op_sel_hi:[1,0]
	v_pk_mul_f32 v[64:65], v[64:65], v[72:73] op_sel_hi:[1,0]
	v_pk_mul_f32 v[62:63], v[62:63], v[72:73] op_sel_hi:[1,0]
	global_store_dwordx4 v[66:67], v[50:53], off
	v_add_u32_e32 v54, 0xa0, v146
	v_ashrrev_i32_e32 v55, 31, v54
	v_cvt_pk_bf16_f32 v50, v58, v59
	v_cvt_pk_bf16_f32 v51, v60, v61
	v_cvt_pk_bf16_f32 v52, v62, v63
	v_cvt_pk_bf16_f32 v53, v64, v65
	global_store_dwordx4 v[66:67], v[50:53], off offset:256
	s_nop 1
	v_mov_b64_e32 v[50:51], v[222:223]
	v_mov_b64_e32 v[52:53], v[224:225]
	v_mov_b32_e32 v56, v51
	v_mov_b32_e32 v57, v52
	v_mov_b32_e32 v51, v53
	v_pk_add_f32 v[50:51], v[56:57], v[50:51]
	v_lshl_add_u64 v[52:53], v[54:55], 4, s[8:9]
	v_add_f32_e32 v50, v50, v51
	v_fmamk_f32 v50, v50, 0x3b800000, v153
	v_rsq_f32_e32 v56, v50
	v_lshlrev_b64 v[50:51], 10, v[70:71]
	v_lshl_add_u64 v[50:51], v[144:145], 0, v[50:51]
	v_mul_f32_e32 v56, v147, v56
	v_pk_mul_f32 v[36:37], v[36:37], v[56:57] op_sel_hi:[1,0]
	v_pk_mul_f32 v[34:35], v[34:35], v[56:57] op_sel_hi:[1,0]
	v_pk_mul_f32 v[40:41], v[40:41], v[56:57] op_sel_hi:[1,0]
	v_pk_mul_f32 v[38:39], v[38:39], v[56:57] op_sel_hi:[1,0]
	v_cvt_pk_bf16_f32 v34, v34, v35
	v_cvt_pk_bf16_f32 v35, v36, v37
	v_pk_mul_f32 v[44:45], v[44:45], v[56:57] op_sel_hi:[1,0]
	v_cvt_pk_bf16_f32 v36, v38, v39
	v_cvt_pk_bf16_f32 v37, v40, v41
	v_pk_mul_f32 v[42:43], v[42:43], v[56:57] op_sel_hi:[1,0]
	v_pk_mul_f32 v[48:49], v[48:49], v[56:57] op_sel_hi:[1,0]
	v_pk_mul_f32 v[46:47], v[46:47], v[56:57] op_sel_hi:[1,0]
	global_store_dwordx4 v[50:51], v[34:37], off
	v_add_u32_e32 v38, 0xb0, v146
	v_ashrrev_i32_e32 v39, 31, v38
	v_cvt_pk_bf16_f32 v34, v42, v43
	v_cvt_pk_bf16_f32 v35, v44, v45
	v_cvt_pk_bf16_f32 v36, v46, v47
	v_cvt_pk_bf16_f32 v37, v48, v49
	global_store_dwordx4 v[50:51], v[34:37], off offset:256
	s_nop 1
	v_mov_b64_e32 v[34:35], v[226:227]
	v_mov_b64_e32 v[36:37], v[228:229]
	v_mov_b32_e32 v40, v35
	v_mov_b32_e32 v41, v36
	v_mov_b32_e32 v35, v37
	v_pk_add_f32 v[34:35], v[40:41], v[34:35]
	v_lshl_add_u64 v[36:37], v[38:39], 4, s[8:9]
	v_add_f32_e32 v34, v34, v35
	v_fmamk_f32 v34, v34, 0x3b800000, v153
	v_rsq_f32_e32 v40, v34
	v_lshlrev_b64 v[34:35], 10, v[54:55]
	v_lshl_add_u64 v[34:35], v[144:145], 0, v[34:35]
	v_mul_f32_e32 v40, v147, v40
	v_pk_mul_f32 v[20:21], v[20:21], v[40:41] op_sel_hi:[1,0]
	v_pk_mul_f32 v[18:19], v[18:19], v[40:41] op_sel_hi:[1,0]
	v_pk_mul_f32 v[24:25], v[24:25], v[40:41] op_sel_hi:[1,0]
	v_pk_mul_f32 v[22:23], v[22:23], v[40:41] op_sel_hi:[1,0]
	v_cvt_pk_bf16_f32 v18, v18, v19
	v_cvt_pk_bf16_f32 v19, v20, v21
	v_pk_mul_f32 v[28:29], v[28:29], v[40:41] op_sel_hi:[1,0]
	v_cvt_pk_bf16_f32 v20, v22, v23
	v_cvt_pk_bf16_f32 v21, v24, v25
	v_pk_mul_f32 v[26:27], v[26:27], v[40:41] op_sel_hi:[1,0]
	v_pk_mul_f32 v[32:33], v[32:33], v[40:41] op_sel_hi:[1,0]
	v_pk_mul_f32 v[30:31], v[30:31], v[40:41] op_sel_hi:[1,0]
	global_store_dwordx4 v[34:35], v[18:21], off
	s_nop 1
	v_cvt_pk_bf16_f32 v18, v26, v27
	v_cvt_pk_bf16_f32 v19, v28, v29
	v_cvt_pk_bf16_f32 v20, v30, v31
	v_cvt_pk_bf16_f32 v21, v32, v33
	global_store_dwordx4 v[34:35], v[18:21], off offset:256
	s_nop 1
	v_mov_b64_e32 v[18:19], v[230:231]
	v_mov_b64_e32 v[20:21], v[232:233]
	v_mov_b32_e32 v22, v19
	v_mov_b32_e32 v23, v20
	v_mov_b32_e32 v19, v21
	v_pk_add_f32 v[18:19], v[22:23], v[18:19]
	s_nop 0
	v_add_f32_e32 v18, v18, v19
	v_fmamk_f32 v18, v18, 0x3b800000, v153
	v_rsq_f32_e32 v20, v18
	v_lshlrev_b64 v[18:19], 10, v[38:39]
	v_lshl_add_u64 v[18:19], v[144:145], 0, v[18:19]
	v_mul_f32_e32 v20, v147, v20
	v_pk_mul_f32 v[4:5], v[4:5], v[20:21] op_sel_hi:[1,0]
	v_pk_mul_f32 v[2:3], v[2:3], v[20:21] op_sel_hi:[1,0]
	v_pk_mul_f32 v[8:9], v[8:9], v[20:21] op_sel_hi:[1,0]
	v_pk_mul_f32 v[6:7], v[6:7], v[20:21] op_sel_hi:[1,0]
	v_cvt_pk_bf16_f32 v2, v2, v3
	v_cvt_pk_bf16_f32 v3, v4, v5
	v_pk_mul_f32 v[12:13], v[12:13], v[20:21] op_sel_hi:[1,0]
	v_cvt_pk_bf16_f32 v4, v6, v7
	v_cvt_pk_bf16_f32 v5, v8, v9
	v_pk_mul_f32 v[10:11], v[10:11], v[20:21] op_sel_hi:[1,0]
	v_pk_mul_f32 v[16:17], v[16:17], v[20:21] op_sel_hi:[1,0]
	v_pk_mul_f32 v[14:15], v[14:15], v[20:21] op_sel_hi:[1,0]
	global_store_dwordx4 v[18:19], v[2:5], off
	s_nop 1
	v_cvt_pk_bf16_f32 v2, v10, v11
	v_cvt_pk_bf16_f32 v3, v12, v13
	v_cvt_pk_bf16_f32 v4, v14, v15
	v_cvt_pk_bf16_f32 v5, v16, v17
	global_store_dwordx4 v[18:19], v[2:5], off offset:256
	s_cbranch_vccnz .LBB0_499
	s_andn2_b64 vcc, exec, s[0:1]
	s_cbranch_vccnz .LBB0_498
	s_barrier
	s_branch .LBB0_498

.LBB0_712:
	s_waitcnt vmcnt(2)
	v_mfma_f32_16x16x32_bf16 v[90:93], v[118:121], v[66:69], 0
	s_add_i32 s1, s0, 2
	s_add_i32 s52, s52, 16
	v_mfma_f32_16x16x32_bf16 v[94:97], v[118:121], v[2:5], 0
	v_mfma_f32_16x16x32_bf16 v[106:109], v[118:121], v[6:9], 0
	v_mfma_f32_16x16x32_bf16 v[90:93], v[114:117], v[70:73], v[90:93]
	v_mfma_f32_16x16x32_bf16 v[132:135], v[118:121], v[10:13], 0
	v_mfma_f32_16x16x32_bf16 v[174:177], v[118:121], v[14:17], 0
	v_mfma_f32_16x16x32_bf16 v[94:97], v[114:117], v[34:37], v[94:97]
	v_mfma_f32_16x16x32_bf16 v[106:109], v[114:117], v[38:41], v[106:109]
	v_mov_b32_e32 v128, s0
	v_add_u32_e32 v112, 0x100, v128
	v_min_u32_e32 v112, 0x1fff, v112
	v_lshlrev_b32_e32 v140, 7, v112
	v_add_u32_e32 v112, 0x110, v128
	v_min_i32_e32 v112, 0x1fff, v112
	v_ashrrev_i32_e32 v113, 31, v112
	v_lshlrev_b64 v[112:113], 7, v[112:113]
	v_lshl_add_u64 v[124:125], v[172:173], 0, v[112:113]
	v_add_u32_e32 v112, 0x120, v128
	v_min_i32_e32 v112, 0x1fff, v112
	v_ashrrev_i32_e32 v113, 31, v112
	v_lshlrev_b64 v[112:113], 7, v[112:113]
	v_lshl_add_u64 v[122:123], v[172:173], 0, v[140:141]
	v_lshl_add_u64 v[126:127], v[172:173], 0, v[112:113]
	v_add_u32_e32 v112, 0x130, v128
	v_mfma_f32_16x16x32_bf16 v[178:181], v[118:121], v[18:21], 0
	v_mfma_f32_16x16x32_bf16 v[182:185], v[118:121], v[22:25], 0
	v_mfma_f32_16x16x32_bf16 v[132:135], v[114:117], v[42:45], v[132:135]
	v_mfma_f32_16x16x32_bf16 v[174:177], v[114:117], v[46:49], v[174:177]
	v_mfma_f32_16x16x32_bf16 v[186:189], v[118:121], v[26:29], 0
	v_mfma_f32_16x16x32_bf16 v[118:121], v[118:121], v[30:33], 0
	v_mfma_f32_16x16x32_bf16 v[178:181], v[114:117], v[50:53], v[178:181]
	v_mfma_f32_16x16x32_bf16 v[182:185], v[114:117], v[54:57], v[182:185]
	v_min_i32_e32 v112, 0x1fff, v112
	v_fma_f32 v90, v156, |v94|, v90
	v_fma_f32 v91, v156, |v95|, v91
	v_fma_f32 v92, v156, |v96|, v92
	v_fma_f32 v93, v156, |v97|, v93
	v_ashrrev_i32_e32 v113, 31, v112
	v_lshlrev_b64 v[112:113], 7, v[112:113]
	v_fma_f32 v90, v158, |v106|, v90
	v_fma_f32 v91, v158, |v107|, v91
	v_fma_f32 v92, v158, |v108|, v92
	v_fma_f32 v93, v158, |v109|, v93
	v_lshl_add_u64 v[128:129], v[172:173], 0, v[112:113]
	s_nop 0
	v_fma_f32 v112, v160, |v132|, v90
	v_fma_f32 v113, v160, |v133|, v91
	v_fma_f32 v131, v160, |v134|, v92
	v_fma_f32 v136, v160, |v135|, v93
	v_mfma_f32_16x16x32_bf16 v[106:109], v[102:105], v[66:69], 0
	v_mfma_f32_16x16x32_bf16 v[90:93], v[114:117], v[58:61], v[186:189]
	v_mfma_f32_16x16x32_bf16 v[94:97], v[114:117], v[62:65], v[118:121]
	v_mfma_f32_16x16x32_bf16 v[114:117], v[98:101], v[70:73], v[106:109]
	v_mfma_f32_16x16x32_bf16 v[106:109], v[102:105], v[2:5], 0
	v_mfma_f32_16x16x32_bf16 v[118:121], v[102:105], v[6:9], 0
	v_mfma_f32_16x16x32_bf16 v[132:135], v[102:105], v[10:13], 0
	v_mfma_f32_16x16x32_bf16 v[186:189], v[102:105], v[14:17], 0
	v_fma_f32 v112, v162, |v174|, v112
	v_fma_f32 v113, v162, |v175|, v113
	v_fma_f32 v131, v162, |v176|, v131
	v_fma_f32 v136, v162, |v177|, v136
	s_nop 0
	v_fma_f32 v112, v164, |v178|, v112
	v_fma_f32 v113, v164, |v179|, v113
	v_fma_f32 v131, v164, |v180|, v131
	v_fma_f32 v136, v164, |v181|, v136
	s_nop 0
	v_fma_f32 v112, v166, |v182|, v112
	v_fma_f32 v113, v166, |v183|, v113
	v_fma_f32 v131, v166, |v184|, v131
	v_fma_f32 v136, v166, |v185|, v136
	s_nop 0
	v_fma_f32 v112, v168, |v90|, v112
	v_fma_f32 v113, v168, |v91|, v113
	v_fma_f32 v131, v168, |v92|, v131
	v_fma_f32 v136, v168, |v93|, v136
	v_mfma_f32_16x16x32_bf16 v[174:177], v[98:101], v[34:37], v[106:109]
	v_mfma_f32_16x16x32_bf16 v[118:121], v[98:101], v[38:41], v[118:121]
	v_mfma_f32_16x16x32_bf16 v[132:135], v[98:101], v[42:45], v[132:135]
	v_mfma_f32_16x16x32_bf16 v[178:181], v[98:101], v[46:49], v[186:189]
	v_mfma_f32_16x16x32_bf16 v[90:93], v[102:105], v[18:21], 0
	v_mfma_f32_16x16x32_bf16 v[182:185], v[102:105], v[22:25], 0
	v_mfma_f32_16x16x32_bf16 v[186:189], v[102:105], v[26:29], 0
	v_mfma_f32_16x16x32_bf16 v[190:193], v[102:105], v[30:33], 0
	v_fma_f32 v94, v170, |v94|, v112
	v_fma_f32 v95, v170, |v95|, v113
	v_fma_f32 v96, v170, |v96|, v131
	v_fma_f32 v97, v170, |v97|, v136
	v_cmp_gt_i32_e32 vcc, s0, v130
	v_cvt_pk_f16_f32 v113, v96, v97
	v_pk_ashrrev_i16 v96, 15, v113 op_sel_hi:[0,1]
	v_cvt_pk_f16_f32 v94, v94, v95
	v_or_b32_e32 v131, 0x80008000, v96
	v_cndmask_b32_e64 v96, v207, 0, vcc
	v_cmp_lt_i32_e32 vcc, s0, v130
	v_pk_ashrrev_i16 v95, 15, v94 op_sel_hi:[0,1]
	v_or_b32_e32 v95, 0x80008000, v95
	v_cndmask_b32_e32 v97, 0, v208, vcc
	v_or_b32_e32 v96, v96, v97
	v_bitop3_b32 v112, v95, v96, v94 bitop3:0x48
	v_mfma_f32_16x16x32_bf16 v[106:109], v[98:101], v[50:53], v[90:93]
	v_mfma_f32_16x16x32_bf16 v[102:105], v[98:101], v[54:57], v[182:185]
	v_mfma_f32_16x16x32_bf16 v[94:97], v[98:101], v[58:61], v[186:189]
	v_mfma_f32_16x16x32_bf16 v[90:93], v[98:101], v[62:65], v[190:193]
	v_mfma_f32_16x16x32_bf16 v[98:101], v[86:89], v[66:69], 0
	v_mfma_f32_16x16x32_bf16 v[182:185], v[82:85], v[70:73], v[98:101]
	v_mfma_f32_16x16x32_bf16 v[98:101], v[86:89], v[2:5], 0
	v_mfma_f32_16x16x32_bf16 v[186:189], v[86:89], v[6:9], 0
	v_cmp_gt_i32_e32 vcc, s1, v130
	s_add_i32 s1, s0, 3
	v_fma_f32 v114, v156, |v174|, v114
	v_cndmask_b32_e64 v136, v207, 0, vcc
	v_cmp_gt_i32_e32 vcc, s1, v130
	v_fma_f32 v115, v156, |v175|, v115
	s_add_i32 s1, s0, 16
	v_cndmask_b32_e64 v137, v208, 0, vcc
	v_or_b32_e32 v136, v136, v137
	v_bitop3_b32 v113, v131, v136, v113 bitop3:0x48
	v_bfe_u32 v131, v112, 7, 9
	v_lshrrev_b32_e32 v136, 23, v112
	v_bfe_u32 v137, v113, 7, 9
	v_lshrrev_b32_e32 v140, 23, v113
	s_nop 0
	v_lshl_add_u32 v131, v131, 2, v143
	v_lshl_add_u32 v136, v136, 2, v143
	v_lshl_add_u32 v137, v137, 2, v143
	v_lshl_add_u32 v140, v140, 2, v143
	v_mfma_f32_16x16x32_bf16 v[190:193], v[86:89], v[10:13], 0
	v_mfma_f32_16x16x32_bf16 v[194:197], v[86:89], v[14:17], 0
	v_mfma_f32_16x16x32_bf16 v[210:213], v[82:85], v[34:37], v[98:101]
	v_mfma_f32_16x16x32_bf16 v[186:189], v[82:85], v[38:41], v[186:189]
	v_mfma_f32_16x16x32_bf16 v[190:193], v[82:85], v[42:45], v[190:193]
	v_mfma_f32_16x16x32_bf16 v[194:197], v[82:85], v[46:49], v[194:197]
	v_mfma_f32_16x16x32_bf16 v[98:101], v[86:89], v[18:21], 0
	v_mfma_f32_16x16x32_bf16 v[224:227], v[86:89], v[22:25], 0
	v_fma_f32 v116, v156, |v176|, v116
	v_fma_f32 v117, v156, |v177|, v117
	s_nop 0
	v_fma_f32 v114, v158, |v118|, v114
	v_fma_f32 v115, v158, |v119|, v115
	v_fma_f32 v116, v158, |v120|, v116
	v_fma_f32 v117, v158, |v121|, v117
	s_nop 0
	v_fma_f32 v114, v160, |v132|, v114
	v_fma_f32 v115, v160, |v133|, v115
	v_fma_f32 v116, v160, |v134|, v116
	v_fma_f32 v117, v160, |v135|, v117
	s_nop 0
	v_fma_f32 v114, v162, |v178|, v114
	v_fma_f32 v115, v162, |v179|, v115
	v_fma_f32 v118, v162, |v180|, v116
	v_fma_f32 v119, v162, |v181|, v117
	s_nop 0
	v_fma_f32 v106, v164, |v106|, v114
	v_fma_f32 v107, v164, |v107|, v115
	v_mfma_f32_16x16x32_bf16 v[114:117], v[86:89], v[26:29], 0
	v_mfma_f32_16x16x32_bf16 v[86:89], v[86:89], v[30:33], 0
	v_mfma_f32_16x16x32_bf16 v[132:135], v[82:85], v[50:53], v[98:101]
	v_mfma_f32_16x16x32_bf16 v[174:177], v[82:85], v[54:57], v[224:227]
	v_mfma_f32_16x16x32_bf16 v[178:181], v[82:85], v[58:61], v[114:117]
	v_mfma_f32_16x16x32_bf16 v[224:227], v[82:85], v[62:65], v[86:89]
	v_mfma_f32_16x16x32_bf16 v[82:85], v[78:81], v[66:69], 0
	v_mfma_f32_16x16x32_bf16 v[228:231], v[74:77], v[70:73], v[82:85]
	s_nop 6
	v_fma_f32 v82, v164, |v108|, v118
	v_fma_f32 v83, v164, |v109|, v119
	global_load_dwordx4 v[118:121], v[122:123], off
	global_load_dwordx4 v[114:117], v[122:123], off offset:1024
	s_nop 0
	v_fma_f32 v84, v166, |v102|, v106
	v_fma_f32 v85, v166, |v103|, v107
	v_fma_f32 v82, v166, |v104|, v82
	v_fma_f32 v83, v166, |v105|, v83
	global_load_dwordx4 v[102:105], v[124:125], off
	global_load_dwordx4 v[98:101], v[124:125], off offset:1024
	s_nop 0
	v_fma_f32 v84, v168, |v94|, v84
	v_fma_f32 v85, v168, |v95|, v85
	v_fma_f32 v82, v168, |v96|, v82
	v_fma_f32 v83, v168, |v97|, v83
	s_nop 0
	v_fma_f32 v84, v170, |v90|, v84
	v_fma_f32 v85, v170, |v91|, v85
	v_fma_f32 v82, v170, |v92|, v82
	v_fma_f32 v83, v170, |v93|, v83
	s_nop 0
	v_cvt_pk_f16_f32 v157, v84, v85
	v_cvt_pk_f16_f32 v159, v82, v83
	v_mfma_f32_16x16x32_bf16 v[82:85], v[78:81], v[2:5], 0
	v_mfma_f32_16x16x32_bf16 v[90:93], v[78:81], v[6:9], 0
	v_mfma_f32_16x16x32_bf16 v[106:109], v[78:81], v[10:13], 0
	v_mfma_f32_16x16x32_bf16 v[232:235], v[78:81], v[14:17], 0
	v_mfma_f32_16x16x32_bf16 v[236:239], v[74:77], v[34:37], v[82:85]
	global_load_dwordx4 v[86:89], v[126:127], off
	global_load_dwordx4 v[82:85], v[126:127], off offset:1024
	v_mfma_f32_16x16x32_bf16 v[122:125], v[74:77], v[38:41], v[90:93]
	global_load_dwordx4 v[94:97], v[128:129], off
	global_load_dwordx4 v[90:93], v[128:129], off offset:1024
	ds_add_u32 v131, v206
	ds_add_u32 v136, v206
	v_mfma_f32_16x16x32_bf16 v[106:109], v[74:77], v[42:45], v[106:109]
	ds_add_u32 v137, v206
	ds_add_u32 v140, v206
	v_mfma_f32_16x16x32_bf16 v[126:129], v[74:77], v[46:49], v[232:235]
	v_pk_ashrrev_i16 v136, 15, v159 op_sel_hi:[0,1]
	v_cmp_gt_i32_e32 vcc, s1, v130
	s_add_i32 s1, s0, 17
	v_or_b32_e32 v137, 0x80008000, v136
	v_cndmask_b32_e64 v136, v207, 0, vcc
	v_cmp_gt_i32_e32 vcc, s1, v130
	v_pk_ashrrev_i16 v131, 15, v157 op_sel_hi:[0,1]
	s_add_i32 s1, s0, 18
	v_cndmask_b32_e64 v140, v208, 0, vcc
	v_or_b32_e32 v131, 0x80008000, v131
	v_or_b32_e32 v136, v136, v140
	v_cmp_gt_i32_e32 vcc, s1, v130
	s_add_i32 s1, s0, 19
	v_bitop3_b32 v136, v131, v136, v157 bitop3:0x48
	v_cndmask_b32_e64 v131, v207, 0, vcc
	v_cmp_gt_i32_e32 vcc, s1, v130
	s_add_i32 s1, s0, 32
	s_nop 0
	v_cndmask_b32_e64 v140, v208, 0, vcc
	v_or_b32_e32 v131, v131, v140
	v_bitop3_b32 v137, v137, v131, v159 bitop3:0x48
	v_bfe_u32 v131, v136, 7, 9
	v_lshrrev_b32_e32 v140, 23, v136
	v_bfe_u32 v157, v137, 7, 9
	v_lshrrev_b32_e32 v159, 23, v137
	v_cmp_gt_i32_e32 vcc, s1, v130
	v_lshl_add_u32 v131, v131, 2, v143
	ds_add_u32 v131, v206
	v_lshl_add_u32 v131, v140, 2, v143
	ds_add_u32 v131, v206
	v_lshl_add_u32 v131, v157, 2, v143
	ds_add_u32 v131, v206
	v_lshl_add_u32 v131, v159, 2, v143
	ds_add_u32 v131, v206
	v_fma_f32 v131, v156, |v210|, v182
	v_fma_f32 v140, v156, |v211|, v183
	v_fma_f32 v157, v156, |v212|, v184
	v_fma_f32 v159, v156, |v213|, v185
	s_add_i32 s1, s0, 33
	v_fma_f32 v131, v158, |v186|, v131
	v_fma_f32 v140, v158, |v187|, v140
	v_fma_f32 v157, v158, |v188|, v157
	v_fma_f32 v159, v158, |v189|, v159
	s_nop 0
	v_fma_f32 v131, v160, |v190|, v131
	v_fma_f32 v140, v160, |v191|, v140
	v_fma_f32 v157, v160, |v192|, v157
	v_fma_f32 v159, v160, |v193|, v159
	s_nop 0
	v_fma_f32 v131, v162, |v194|, v131
	v_fma_f32 v140, v162, |v195|, v140
	v_fma_f32 v157, v162, |v196|, v157
	v_fma_f32 v159, v162, |v197|, v159
	s_nop 0
	v_fma_f32 v131, v164, |v132|, v131
	v_fma_f32 v132, v164, |v133|, v140
	v_fma_f32 v133, v164, |v134|, v157
	v_fma_f32 v134, v164, |v135|, v159
	v_cndmask_b32_e64 v135, v207, 0, vcc
	v_fma_f32 v131, v166, |v174|, v131
	v_fma_f32 v132, v166, |v175|, v132
	v_fma_f32 v133, v166, |v176|, v133
	v_fma_f32 v134, v166, |v177|, v134
	v_cmp_gt_i32_e32 vcc, s1, v130
	v_fma_f32 v131, v168, |v178|, v131
	v_fma_f32 v132, v168, |v179|, v132
	v_fma_f32 v133, v168, |v180|, v133
	v_fma_f32 v134, v168, |v181|, v134
	v_cndmask_b32_e64 v140, v208, 0, vcc
	v_fma_f32 v131, v170, |v224|, v131
	v_fma_f32 v132, v170, |v225|, v132
	v_fma_f32 v133, v170, |v226|, v133
	v_fma_f32 v134, v170, |v227|, v134
	s_add_i32 s1, s0, 34
	v_cvt_pk_f16_f32 v131, v131, v132
	v_cvt_pk_f16_f32 v132, v133, v134
	v_pk_ashrrev_i16 v133, 15, v131 op_sel_hi:[0,1]
	v_or_b32_e32 v133, 0x80008000, v133
	v_or_b32_e32 v135, v135, v140
	v_cmp_gt_i32_e32 vcc, s1, v130
	s_add_i32 s1, s0, 35
	v_bitop3_b32 v182, v133, v135, v131 bitop3:0x48
	v_cndmask_b32_e64 v131, v207, 0, vcc
	v_cmp_gt_i32_e32 vcc, s1, v130
	v_pk_ashrrev_i16 v134, 15, v132 op_sel_hi:[0,1]
	v_or_b32_e32 v134, 0x80008000, v134
	v_cndmask_b32_e64 v133, v208, 0, vcc
	v_or_b32_e32 v131, v131, v133
	v_bitop3_b32 v183, v134, v131, v132 bitop3:0x48
	v_bfe_u32 v131, v182, 7, 9
	v_lshrrev_b32_e32 v132, 23, v182
	v_bfe_u32 v133, v183, 7, 9
	v_lshrrev_b32_e32 v134, 23, v183
	v_fma_f32 v140, v156, |v237|, v229
	v_lshl_add_u32 v131, v131, 2, v143
	ds_add_u32 v131, v206
	v_lshl_add_u32 v131, v132, 2, v143
	ds_add_u32 v131, v206
	v_lshl_add_u32 v131, v133, 2, v143
	ds_add_u32 v131, v206
	v_lshl_add_u32 v131, v134, 2, v143
	v_mfma_f32_16x16x32_bf16 v[132:135], v[78:81], v[18:21], 0
	ds_add_u32 v131, v206
	v_fma_f32 v131, v156, |v236|, v228
	v_fma_f32 v157, v156, |v238|, v230
	v_fma_f32 v159, v156, |v239|, v231
	v_mfma_f32_16x16x32_bf16 v[174:177], v[78:81], v[22:25], 0
	v_fma_f32 v122, v158, |v122|, v131
	v_fma_f32 v131, v158, |v123|, v140
	v_fma_f32 v140, v158, |v124|, v157
	v_fma_f32 v157, v158, |v125|, v159
	v_mfma_f32_16x16x32_bf16 v[178:181], v[78:81], v[26:29], 0
	v_fma_f32 v159, v160, |v106|, v122
	v_fma_f32 v131, v160, |v107|, v131
	v_fma_f32 v140, v160, |v108|, v140
	v_mfma_f32_16x16x32_bf16 v[78:81], v[78:81], v[30:33], 0
	v_fma_f32 v157, v160, |v109|, v157
	s_add_i32 s1, s0, 48
	v_mfma_f32_16x16x32_bf16 v[122:125], v[74:77], v[50:53], v[132:135]
	v_fma_f32 v126, v162, |v126|, v159
	v_fma_f32 v127, v162, |v127|, v131
	v_fma_f32 v128, v162, |v128|, v140
	v_mfma_f32_16x16x32_bf16 v[106:109], v[74:77], v[54:57], v[174:177]
	v_fma_f32 v129, v162, |v129|, v157
	v_cmp_gt_i32_e32 vcc, s1, v130
	v_mfma_f32_16x16x32_bf16 v[132:135], v[74:77], v[58:61], v[178:181]
	s_add_i32 s1, s0, 49
	v_mfma_f32_16x16x32_bf16 v[74:77], v[74:77], v[62:65], v[78:81]
	s_nop 2
	v_fma_f32 v78, v164, |v122|, v126
	v_fma_f32 v79, v164, |v123|, v127
	v_fma_f32 v80, v164, |v124|, v128
	v_fma_f32 v81, v164, |v125|, v129
	s_nop 0
	v_fma_f32 v78, v166, |v106|, v78
	v_fma_f32 v79, v166, |v107|, v79
	v_fma_f32 v80, v166, |v108|, v80
	v_fma_f32 v81, v166, |v109|, v81
	s_nop 0
	v_fma_f32 v78, v168, |v132|, v78
	v_fma_f32 v79, v168, |v133|, v79
	v_fma_f32 v80, v168, |v134|, v80
	v_fma_f32 v81, v168, |v135|, v81
	s_nop 0
	v_fma_f32 v74, v170, |v74|, v78
	v_fma_f32 v75, v170, |v75|, v79
	v_fma_f32 v76, v170, |v76|, v80
	v_fma_f32 v77, v170, |v77|, v81
	v_cndmask_b32_e64 v78, v207, 0, vcc
	v_cvt_pk_f16_f32 v74, v74, v75
	v_cmp_gt_i32_e32 vcc, s1, v130
	v_cvt_pk_f16_f32 v75, v76, v77
	v_pk_ashrrev_i16 v76, 15, v74 op_sel_hi:[0,1]
	v_cndmask_b32_e64 v79, v208, 0, vcc
	s_add_i32 s1, s0, 50
	v_or_b32_e32 v76, 0x80008000, v76
	v_or_b32_e32 v78, v78, v79
	v_cmp_gt_i32_e32 vcc, s1, v130
	s_add_i32 s1, s0, 51
	v_bitop3_b32 v74, v76, v78, v74 bitop3:0x48
	v_cndmask_b32_e64 v76, v207, 0, vcc
	v_cmp_gt_i32_e32 vcc, s1, v130
	v_pk_ashrrev_i16 v77, 15, v75 op_sel_hi:[0,1]
	v_or_b32_e32 v77, 0x80008000, v77
	v_cndmask_b32_e64 v78, v208, 0, vcc
	v_or_b32_e32 v76, v76, v78
	v_bitop3_b32 v75, v77, v76, v75 bitop3:0x48
	v_bfe_u32 v76, v74, 7, 9
	v_lshrrev_b32_e32 v77, 23, v74
	v_bfe_u32 v78, v75, 7, 9
	v_lshrrev_b32_e32 v79, 23, v75
	s_addk_i32 s0, 0x100
	v_lshl_add_u32 v76, v76, 2, v143
	ds_add_u32 v76, v206
	v_lshl_add_u32 v76, v77, 2, v143
	ds_add_u32 v76, v206
	v_lshl_add_u32 v76, v78, 2, v143
	ds_add_u32 v76, v206
	v_lshl_add_u32 v76, v79, 2, v143
	ds_add_u32 v76, v206
	v_add_u32_e32 v76, v201, v142
	ds_write2_b64 v76, v[112:113], v[136:137] offset1:4
	ds_write2_b64 v76, v[182:183], v[74:75] offset0:8 offset1:12
	s_waitcnt lgkmcnt(0)
	v_add_u32_e32 v78, v202, v203
	ds_read_b128 v[74:77], v78
	ds_read_b128 v[78:81], v78 offset:1152
	s_cmp_lt_i32 s52, s8
	s_waitcnt lgkmcnt(1)
	global_store_dwordx4 v[110:111], v[74:77], off
	s_nop 1
	v_add_co_u32_e32 v74, vcc, 0x20000, v110
	s_nop 1
	v_addc_co_u32_e32 v75, vcc, 0, v111, vcc
	s_waitcnt lgkmcnt(0)
	global_store_dwordx4 v[74:75], v[78:81], off
	s_waitcnt lgkmcnt(0)
	v_lshl_add_u64 v[110:111], v[110:111], 0, s[14:15]
	v_mov_b64_e32 v[74:75], v[90:91]
	v_mov_b64_e32 v[78:79], v[94:95]
	v_mov_b64_e32 v[80:81], v[96:97]
	v_mov_b64_e32 v[76:77], v[92:93]
	s_cbranch_scc1 .LBB0_712
